# baseline (speedup 1.0000x reference)
.Lpf_kv:
	s_lshr_b32 s8, s3, 2
	s_add_u32 s21, s8, 1
	s_and_b32 s8, s3, 3
	s_and_b32 s9, s8, 1
	s_lshr_b32 s8, s8, 1
	s_lshl_b32 s8, s8, 1
	s_add_u32 s8, s8, s6
	s_cmp_eq_u32 s21, 1
	s_cselect_b32 s12, s26, s28
	s_cselect_b32 s13, s27, s29
	s_cselect_b32 s14, s36, s38
	s_cselect_b32 s15, s37, s39
	s_mov_b32 s16, s42
	s_mov_b32 s17, s43
	s_cselect_b32 s22, s46, s48
	s_cselect_b32 s23, s47, s49
	s_mov_b32 s19, 1.0
	s_waitcnt lgkmcnt(0)
	s_cmp_eq_u32 s9, 0
	s_cselect_b32 s51, s52, s53
	s_movk_i32 s54, 0x100
	s_movk_i32 s55, 0x120
	s_cmp_le_i32 s51, 0x400
	s_cselect_b32 s55, s54, s55
	s_mul_i32 s10, s8, s55
	s_lshl_b32 s11, s9, 11
	s_add_u32 s11, s11, s10
	s_cmp_ge_i32 s10, s51
	s_cbranch_scc1 .Lpf_done
.Lpf_common:
	s_mul_i32 s8, s11, 0x880
	s_mul_hi_u32 s24, s11, 0x880
	s_add_u32 s12, s12, s8
	s_addc_u32 s13, s13, s24
	s_lshl_b32 s8, s21, 10
	s_lshl_b32 s24, s5, 7
	s_add_u32 s8, s8, s24
	s_mul_i32 s8, s8, 0x880
	s_add_u32 s6, s30, s8
	s_addc_u32 s7, s31, 0
	s_mov_b32 s4, s12
	s_mov_b32 s5, s13
	s_and_b32 s24, s18, 1
	s_lshr_b32 s25, s18, 1
	s_lshr_b32 s26, s2, 3
	s_and_b32 s26, s26, 7
	s_lshl_b32 s26, s26, 1
	s_add_u32 s26, s26, s24
	s_lshl_b32 s27, s9, 4
	s_add_u32 s27, s27, s26
	s_lshl_b32 s28, s18, 10
	s_lshl_b32 s8, s26, 8
	s_add_u32 s14, s14, s8
	s_addc_u32 s15, s15, 0
	s_lshl_b32 s8, s27, 18
	s_add_u32 s22, s22, s8
	s_addc_u32 s23, s23, 0
	v_lshrrev_b32_e32 v5, 3, v1
	v_lshl_add_u32 v5, v2, 3, v5
	v_mul_u32_u24_e32 v5, 0x880, v5
	v_and_b32_e32 v6, 7, v1
	v_lshrrev_b32_e32 v7, 4, v1
	v_and_b32_e32 v8, 1, v2
	v_lshl_or_b32 v7, v8, 2, v7
	v_xor_b32_e32 v6, v6, v7
	v_lshl_add_u32 v10, v6, 4, v5
	v_add_u32_e32 v11, 0x22000, v10
	v_add_u32_e32 v12, 0x44000, v10
	v_add_u32_e32 v13, 0x66000, v10
	v_add_u32_e32 v14, 0x88000, v10
	v_lshrrev_b32_e32 v5, 1, v3
	v_xor_b32_e32 v6, v4, v5
	v_lshlrev_b32_e32 v6, 4, v6
	v_or_b32_e32 v7, 4, v4
	v_xor_b32_e32 v7, v7, v5
	v_lshlrev_b32_e32 v7, 4, v7
	v_lshl_add_u32 v9, v8, 6, v3
	v_lshlrev_b32_e32 v9, 7, v9
	v_and_b32_e32 v5, 1, v4
	v_lshl_add_u32 v5, v5, 5, v3
	v_lshlrev_b32_e32 v5, 4, v5
	v_lshrrev_b32_e32 v8, 1, v4
	v_lshl_add_u32 v23, v8, 3, v5
	s_cmp_eq_u32 s21, 0
	s_cbranch_scc1 .Lpf_vQ
	s_cmp_eq_u32 s55, 0x100
	s_cbranch_scc0 .Lpf_v288
	s_cmp_eq_u32 s21, 1
	s_cbranch_scc1 .Lpf_vQ
	s_branch .Lpf_vV256
.Lpf_v288:
	s_cmp_lt_u32 s18, 4
	s_cselect_b32 s8, 1, 0
	s_cmp_eq_u32 s21, 1
	s_cbranch_scc0 .Lpf_vV
	s_cmp_eq_u32 s8, 1
	s_cbranch_scc1 .Lpf_vKA
	s_branch .Lpf_vKB

.Lpf_vV256:
	s_lshl_b32 s25, s25, 6
	s_add_u32 s29, s10, s25
	s_lshr_b32 s29, s29, 4
	v_add_u32_e32 v5, s25, v3
	v_lshlrev_b32_e32 v5, 7, v5
	v_add_u32_e32 v15, v5, v6
	v_add_u32_e32 v16, v5, v7
	v_add_u32_e32 v5, 0x8000, v9
	v_add_u32_e32 v17, v5, v6
	v_add_u32_e32 v18, v5, v7
	v_add_u32_e32 v19, 0x18000, v15
	v_add_u32_e32 v20, 0x18000, v16
	v_add_u32_e32 v21, 0x18000, v17
	v_add_u32_e32 v22, 0x18000, v18
	v_lshlrev_b32_e32 v5, 2, v3
	global_load_dword v24, v5, s[14:15] offset:0
	global_load_dword v26, v5, s[14:15] offset:64
	global_load_dword v28, v5, s[14:15] offset:128
	global_load_dword v30, v5, s[14:15] offset:192
	s_add_u32 m0, s28, 0x0
	s_nop 0
	global_load_lds_dwordx4 v10, s[4:5]
	s_add_u32 m0, s28, 0x2000
	s_nop 0
	global_load_lds_dwordx4 v11, s[4:5]
	s_add_u32 m0, s28, 0x4000
	s_nop 0
	global_load_lds_dwordx4 v12, s[4:5]
	s_add_u32 m0, s28, 0x6000
	s_nop 0
	global_load_lds_dwordx4 v13, s[4:5]
	s_add_u32 s4, s4, s20
	s_addc_u32 s5, s5, 0
	s_add_u32 m0, s28, 0x8000
	s_nop 0
	global_load_lds_dwordx4 v10, s[6:7]
	s_add_u32 m0, s28, 0xa000
	s_nop 0
	global_load_lds_dwordx4 v11, s[6:7]
	s_add_u32 s6, s6, s20
	s_addc_u32 s7, s7, 0
	s_add_u32 m0, s28, 0xc000
	s_nop 0
	global_load_lds_dwordx4 v10, s[4:5]
	s_add_u32 m0, s28, 0xe000
	s_nop 0
	global_load_lds_dwordx4 v11, s[4:5]
	s_add_u32 m0, s28, 0x10000
	s_nop 0
	global_load_lds_dwordx4 v12, s[4:5]
	s_add_u32 m0, s28, 0x12000
	s_nop 0
	global_load_lds_dwordx4 v13, s[4:5]
	s_add_u32 s4, s4, s20
	s_addc_u32 s5, s5, 0
	s_add_u32 m0, s28, 0x14000
	s_nop 0
	global_load_lds_dwordx4 v10, s[6:7]
	s_add_u32 m0, s28, 0x16000
	s_nop 0
	global_load_lds_dwordx4 v11, s[6:7]
	s_add_u32 s6, s6, s20
	s_addc_u32 s7, s7, 0
	s_add_u32 m0, s28, 0x18000
	s_nop 0
	global_load_lds_dwordx4 v10, s[4:5]
	s_add_u32 m0, s28, 0x1a000
	s_nop 0
	global_load_lds_dwordx4 v11, s[4:5]
	s_add_u32 m0, s28, 0x1c000
	s_nop 0
	global_load_lds_dwordx4 v12, s[4:5]
	s_add_u32 m0, s28, 0x1e000
	s_nop 0
	global_load_lds_dwordx4 v13, s[4:5]
	s_add_u32 s4, s4, s20
	s_addc_u32 s5, s5, 0
	s_add_u32 m0, s28, 0x20000
	s_nop 0
	global_load_lds_dwordx4 v10, s[6:7]
	s_add_u32 m0, s28, 0x22000
	s_nop 0
	global_load_lds_dwordx4 v11, s[6:7]
	s_add_u32 s6, s6, s20
	s_addc_u32 s7, s7, 0
	s_waitcnt vmcnt(12) lgkmcnt(0)
	s_barrier
	s_waitcnt lgkmcnt(7)
	ds_read_b128 v[136:139], v15
	ds_read_b128 v[156:159], v17
	ds_read_b128 v[160:163], v17 offset:2048
	ds_read_b128 v[164:167], v17 offset:4096
	ds_read_b128 v[168:171], v17 offset:6144
	ds_read_b128 v[140:143], v15 offset:2048
	ds_read_b128 v[144:147], v15 offset:4096
	ds_read_b128 v[148:151], v15 offset:6144
	s_waitcnt lgkmcnt(7)
	ds_read_b128 v[172:175], v16
	ds_read_b128 v[192:195], v18
	ds_read_b128 v[196:199], v18 offset:2048
	ds_read_b128 v[200:203], v18 offset:4096
	ds_read_b128 v[204:207], v18 offset:6144
	ds_read_b128 v[176:179], v16 offset:2048
	ds_read_b128 v[180:183], v16 offset:4096
	ds_read_b128 v[184:187], v16 offset:6144
	s_waitcnt lgkmcnt(14)
	v_mfma_f32_16x16x32_f16 v[56:59], v[136:139], v[156:159], 0
	s_waitcnt lgkmcnt(13)
	v_mfma_f32_16x16x32_f16 v[60:63], v[136:139], v[160:163], 0
	s_waitcnt lgkmcnt(12)
	v_mfma_f32_16x16x32_f16 v[64:67], v[136:139], v[164:167], 0
	s_waitcnt lgkmcnt(11)
	v_mfma_f32_16x16x32_f16 v[68:71], v[136:139], v[168:171], 0
	s_waitcnt lgkmcnt(10)
	v_mfma_f32_16x16x32_f16 v[72:75], v[140:143], v[156:159], 0
	v_mfma_f32_16x16x32_f16 v[76:79], v[140:143], v[160:163], 0
	v_mfma_f32_16x16x32_f16 v[80:83], v[140:143], v[164:167], 0
	v_mfma_f32_16x16x32_f16 v[84:87], v[140:143], v[168:171], 0
	s_waitcnt lgkmcnt(9)
	v_mfma_f32_16x16x32_f16 v[88:91], v[144:147], v[156:159], 0
	v_mfma_f32_16x16x32_f16 v[92:95], v[144:147], v[160:163], 0
	v_mfma_f32_16x16x32_f16 v[96:99], v[144:147], v[164:167], 0
	v_mfma_f32_16x16x32_f16 v[100:103], v[144:147], v[168:171], 0
	s_waitcnt lgkmcnt(8)
	v_mfma_f32_16x16x32_f16 v[104:107], v[148:151], v[156:159], 0
	v_mfma_f32_16x16x32_f16 v[108:111], v[148:151], v[160:163], 0
	v_mfma_f32_16x16x32_f16 v[112:115], v[148:151], v[164:167], 0
	v_mfma_f32_16x16x32_f16 v[116:119], v[148:151], v[168:171], 0
	s_waitcnt vmcnt(6) lgkmcnt(0)
	s_barrier
	s_waitcnt lgkmcnt(7)
	ds_read_b128 v[136:139], v15 offset:49152
	ds_read_b128 v[156:159], v17 offset:49152
	ds_read_b128 v[160:163], v17 offset:51200
	ds_read_b128 v[164:167], v17 offset:53248
	ds_read_b128 v[168:171], v17 offset:55296
	ds_read_b128 v[140:143], v15 offset:51200
	ds_read_b128 v[144:147], v15 offset:53248
	ds_read_b128 v[148:151], v15 offset:55296
	s_waitcnt lgkmcnt(14)
	v_mfma_f32_16x16x32_f16 v[56:59], v[172:175], v[192:195], v[56:59]
	s_add_u32 m0, s28, 0x0
	s_nop 0
	global_load_lds_dwordx4 v10, s[4:5]
	s_waitcnt lgkmcnt(13)
	v_mfma_f32_16x16x32_f16 v[60:63], v[172:175], v[196:199], v[60:63]
	s_waitcnt lgkmcnt(12)
	v_mfma_f32_16x16x32_f16 v[64:67], v[172:175], v[200:203], v[64:67]
	s_waitcnt lgkmcnt(11)
	v_mfma_f32_16x16x32_f16 v[68:71], v[172:175], v[204:207], v[68:71]
	s_waitcnt lgkmcnt(10)
	v_mfma_f32_16x16x32_f16 v[72:75], v[176:179], v[192:195], v[72:75]
	v_mfma_f32_16x16x32_f16 v[76:79], v[176:179], v[196:199], v[76:79]
	s_add_u32 m0, s28, 0x2000
	s_nop 0
	global_load_lds_dwordx4 v11, s[4:5]
	v_mfma_f32_16x16x32_f16 v[80:83], v[176:179], v[200:203], v[80:83]
	v_mfma_f32_16x16x32_f16 v[84:87], v[176:179], v[204:207], v[84:87]
	s_waitcnt lgkmcnt(9)
	v_mfma_f32_16x16x32_f16 v[88:91], v[180:183], v[192:195], v[88:91]
	v_mfma_f32_16x16x32_f16 v[92:95], v[180:183], v[196:199], v[92:95]
	v_mfma_f32_16x16x32_f16 v[96:99], v[180:183], v[200:203], v[96:99]
	s_add_u32 m0, s28, 0x4000
	s_nop 0
	global_load_lds_dwordx4 v12, s[4:5]
	v_mfma_f32_16x16x32_f16 v[100:103], v[180:183], v[204:207], v[100:103]
	s_waitcnt lgkmcnt(8)
	v_mfma_f32_16x16x32_f16 v[104:107], v[184:187], v[192:195], v[104:107]
	v_mfma_f32_16x16x32_f16 v[108:111], v[184:187], v[196:199], v[108:111]
	v_mfma_f32_16x16x32_f16 v[112:115], v[184:187], v[200:203], v[112:115]
	v_mfma_f32_16x16x32_f16 v[116:119], v[184:187], v[204:207], v[116:119]
	s_waitcnt lgkmcnt(7)
	ds_read_b128 v[172:175], v16 offset:49152
	ds_read_b128 v[192:195], v18 offset:49152
	ds_read_b128 v[196:199], v18 offset:51200
	ds_read_b128 v[200:203], v18 offset:53248
	ds_read_b128 v[204:207], v18 offset:55296
	ds_read_b128 v[176:179], v16 offset:51200
	ds_read_b128 v[180:183], v16 offset:53248
	ds_read_b128 v[184:187], v16 offset:55296
	s_waitcnt lgkmcnt(14)
	v_mfma_f32_16x16x32_f16 v[56:59], v[136:139], v[156:159], v[56:59]
	s_add_u32 m0, s28, 0x6000
	s_nop 0
	global_load_lds_dwordx4 v13, s[4:5]
	s_add_u32 s4, s4, s20
	s_addc_u32 s5, s5, 0
	s_waitcnt lgkmcnt(13)
	v_mfma_f32_16x16x32_f16 v[60:63], v[136:139], v[160:163], v[60:63]
	s_waitcnt lgkmcnt(12)
	v_mfma_f32_16x16x32_f16 v[64:67], v[136:139], v[164:167], v[64:67]
	s_waitcnt lgkmcnt(11)
	v_mfma_f32_16x16x32_f16 v[68:71], v[136:139], v[168:171], v[68:71]
	s_waitcnt lgkmcnt(10)
	v_mfma_f32_16x16x32_f16 v[72:75], v[140:143], v[156:159], v[72:75]
	v_mfma_f32_16x16x32_f16 v[76:79], v[140:143], v[160:163], v[76:79]
	s_add_u32 m0, s28, 0x8000
	s_nop 0
	global_load_lds_dwordx4 v10, s[6:7]
	v_mfma_f32_16x16x32_f16 v[80:83], v[140:143], v[164:167], v[80:83]
	v_mfma_f32_16x16x32_f16 v[84:87], v[140:143], v[168:171], v[84:87]
	s_waitcnt lgkmcnt(9)
	v_mfma_f32_16x16x32_f16 v[88:91], v[144:147], v[156:159], v[88:91]
	v_mfma_f32_16x16x32_f16 v[92:95], v[144:147], v[160:163], v[92:95]
	v_mfma_f32_16x16x32_f16 v[96:99], v[144:147], v[164:167], v[96:99]
	s_add_u32 m0, s28, 0xa000
	s_nop 0
	global_load_lds_dwordx4 v11, s[6:7]
	s_add_u32 s6, s6, s20
	s_addc_u32 s7, s7, 0
	v_mfma_f32_16x16x32_f16 v[100:103], v[144:147], v[168:171], v[100:103]
	s_waitcnt lgkmcnt(8)
	v_mfma_f32_16x16x32_f16 v[104:107], v[148:151], v[156:159], v[104:107]
	v_mfma_f32_16x16x32_f16 v[108:111], v[148:151], v[160:163], v[108:111]
	v_mfma_f32_16x16x32_f16 v[112:115], v[148:151], v[164:167], v[112:115]
	v_mfma_f32_16x16x32_f16 v[116:119], v[148:151], v[168:171], v[116:119]
	s_waitcnt vmcnt(6) lgkmcnt(0)
	s_barrier
	s_waitcnt lgkmcnt(7)
	ds_read_b128 v[136:139], v19
	ds_read_b128 v[156:159], v21
	ds_read_b128 v[160:163], v21 offset:2048
	ds_read_b128 v[164:167], v21 offset:4096
	ds_read_b128 v[168:171], v21 offset:6144
	ds_read_b128 v[140:143], v19 offset:2048
	ds_read_b128 v[144:147], v19 offset:4096
	ds_read_b128 v[148:151], v19 offset:6144
	s_waitcnt lgkmcnt(14)
	v_mfma_f32_16x16x32_f16 v[56:59], v[172:175], v[192:195], v[56:59]
	s_add_u32 m0, s28, 0xc000
	s_nop 0
	global_load_lds_dwordx4 v10, s[4:5]
	s_waitcnt lgkmcnt(13)
	v_mfma_f32_16x16x32_f16 v[60:63], v[172:175], v[196:199], v[60:63]
	s_waitcnt lgkmcnt(12)
	v_mfma_f32_16x16x32_f16 v[64:67], v[172:175], v[200:203], v[64:67]
	s_waitcnt lgkmcnt(11)
	v_mfma_f32_16x16x32_f16 v[68:71], v[172:175], v[204:207], v[68:71]
	s_waitcnt lgkmcnt(10)
	v_mfma_f32_16x16x32_f16 v[72:75], v[176:179], v[192:195], v[72:75]
	v_mfma_f32_16x16x32_f16 v[76:79], v[176:179], v[196:199], v[76:79]
	s_add_u32 m0, s28, 0xe000
	s_nop 0
	global_load_lds_dwordx4 v11, s[4:5]
	v_mfma_f32_16x16x32_f16 v[80:83], v[176:179], v[200:203], v[80:83]
	v_mfma_f32_16x16x32_f16 v[84:87], v[176:179], v[204:207], v[84:87]
	s_waitcnt lgkmcnt(9)
	v_mfma_f32_16x16x32_f16 v[88:91], v[180:183], v[192:195], v[88:91]
	v_mfma_f32_16x16x32_f16 v[92:95], v[180:183], v[196:199], v[92:95]
	v_mfma_f32_16x16x32_f16 v[96:99], v[180:183], v[200:203], v[96:99]
	s_add_u32 m0, s28, 0x10000
	s_nop 0
	global_load_lds_dwordx4 v12, s[4:5]
	v_mfma_f32_16x16x32_f16 v[100:103], v[180:183], v[204:207], v[100:103]
	s_waitcnt lgkmcnt(8)
	v_mfma_f32_16x16x32_f16 v[104:107], v[184:187], v[192:195], v[104:107]
	v_mfma_f32_16x16x32_f16 v[108:111], v[184:187], v[196:199], v[108:111]
	v_mfma_f32_16x16x32_f16 v[112:115], v[184:187], v[200:203], v[112:115]
	v_mfma_f32_16x16x32_f16 v[116:119], v[184:187], v[204:207], v[116:119]
	s_waitcnt lgkmcnt(7)
	ds_read_b128 v[172:175], v20
	ds_read_b128 v[192:195], v22
	ds_read_b128 v[196:199], v22 offset:2048
	ds_read_b128 v[200:203], v22 offset:4096
	ds_read_b128 v[204:207], v22 offset:6144
	ds_read_b128 v[176:179], v20 offset:2048
	ds_read_b128 v[180:183], v20 offset:4096
	ds_read_b128 v[184:187], v20 offset:6144
	s_waitcnt lgkmcnt(14)
	v_mfma_f32_16x16x32_f16 v[56:59], v[136:139], v[156:159], v[56:59]
	s_add_u32 m0, s28, 0x12000
	s_nop 0
	global_load_lds_dwordx4 v13, s[4:5]
	s_add_u32 s4, s4, s20
	s_addc_u32 s5, s5, 0
	s_waitcnt lgkmcnt(13)
	v_mfma_f32_16x16x32_f16 v[60:63], v[136:139], v[160:163], v[60:63]
	s_waitcnt lgkmcnt(12)
	v_mfma_f32_16x16x32_f16 v[64:67], v[136:139], v[164:167], v[64:67]
	s_waitcnt lgkmcnt(11)
	v_mfma_f32_16x16x32_f16 v[68:71], v[136:139], v[168:171], v[68:71]
	s_waitcnt lgkmcnt(10)
	v_mfma_f32_16x16x32_f16 v[72:75], v[140:143], v[156:159], v[72:75]
	v_mfma_f32_16x16x32_f16 v[76:79], v[140:143], v[160:163], v[76:79]
	s_add_u32 m0, s28, 0x14000
	s_nop 0
	global_load_lds_dwordx4 v10, s[6:7]
	v_mfma_f32_16x16x32_f16 v[80:83], v[140:143], v[164:167], v[80:83]
	v_mfma_f32_16x16x32_f16 v[84:87], v[140:143], v[168:171], v[84:87]
	s_waitcnt lgkmcnt(9)
	v_mfma_f32_16x16x32_f16 v[88:91], v[144:147], v[156:159], v[88:91]
	v_mfma_f32_16x16x32_f16 v[92:95], v[144:147], v[160:163], v[92:95]
	v_mfma_f32_16x16x32_f16 v[96:99], v[144:147], v[164:167], v[96:99]
	s_add_u32 m0, s28, 0x16000
	s_nop 0
	global_load_lds_dwordx4 v11, s[6:7]
	s_add_u32 s6, s6, s20
	s_addc_u32 s7, s7, 0
	v_mfma_f32_16x16x32_f16 v[100:103], v[144:147], v[168:171], v[100:103]
	s_waitcnt lgkmcnt(8)
	v_mfma_f32_16x16x32_f16 v[104:107], v[148:151], v[156:159], v[104:107]
	v_mfma_f32_16x16x32_f16 v[108:111], v[148:151], v[160:163], v[108:111]
	v_mfma_f32_16x16x32_f16 v[112:115], v[148:151], v[164:167], v[112:115]
	v_mfma_f32_16x16x32_f16 v[116:119], v[148:151], v[168:171], v[116:119]
	s_waitcnt vmcnt(6) lgkmcnt(0)
	s_barrier
	s_waitcnt lgkmcnt(7)
	ds_read_b128 v[136:139], v15
	ds_read_b128 v[156:159], v17
	ds_read_b128 v[160:163], v17 offset:2048
	ds_read_b128 v[164:167], v17 offset:4096
	ds_read_b128 v[168:171], v17 offset:6144
	ds_read_b128 v[140:143], v15 offset:2048
	ds_read_b128 v[144:147], v15 offset:4096
	ds_read_b128 v[148:151], v15 offset:6144
	s_waitcnt lgkmcnt(14)
	v_mfma_f32_16x16x32_f16 v[56:59], v[172:175], v[192:195], v[56:59]
	s_add_u32 m0, s28, 0x18000
	s_nop 0
	global_load_lds_dwordx4 v10, s[4:5]
	s_waitcnt lgkmcnt(13)
	v_mfma_f32_16x16x32_f16 v[60:63], v[172:175], v[196:199], v[60:63]
	s_waitcnt lgkmcnt(12)
	v_mfma_f32_16x16x32_f16 v[64:67], v[172:175], v[200:203], v[64:67]
	s_waitcnt lgkmcnt(11)
	v_mfma_f32_16x16x32_f16 v[68:71], v[172:175], v[204:207], v[68:71]
	s_waitcnt lgkmcnt(10)
	v_mfma_f32_16x16x32_f16 v[72:75], v[176:179], v[192:195], v[72:75]
	v_mfma_f32_16x16x32_f16 v[76:79], v[176:179], v[196:199], v[76:79]
	s_add_u32 m0, s28, 0x1a000
	s_nop 0
	global_load_lds_dwordx4 v11, s[4:5]
	v_mfma_f32_16x16x32_f16 v[80:83], v[176:179], v[200:203], v[80:83]
	v_mfma_f32_16x16x32_f16 v[84:87], v[176:179], v[204:207], v[84:87]
	s_waitcnt lgkmcnt(9)
	v_mfma_f32_16x16x32_f16 v[88:91], v[180:183], v[192:195], v[88:91]
	v_mfma_f32_16x16x32_f16 v[92:95], v[180:183], v[196:199], v[92:95]
	v_mfma_f32_16x16x32_f16 v[96:99], v[180:183], v[200:203], v[96:99]
	s_add_u32 m0, s28, 0x1c000
	s_nop 0
	global_load_lds_dwordx4 v12, s[4:5]
	v_mfma_f32_16x16x32_f16 v[100:103], v[180:183], v[204:207], v[100:103]
	s_waitcnt lgkmcnt(8)
	v_mfma_f32_16x16x32_f16 v[104:107], v[184:187], v[192:195], v[104:107]
	v_mfma_f32_16x16x32_f16 v[108:111], v[184:187], v[196:199], v[108:111]
	v_mfma_f32_16x16x32_f16 v[112:115], v[184:187], v[200:203], v[112:115]
	v_mfma_f32_16x16x32_f16 v[116:119], v[184:187], v[204:207], v[116:119]
	s_waitcnt lgkmcnt(7)
	ds_read_b128 v[172:175], v16
	ds_read_b128 v[192:195], v18
	ds_read_b128 v[196:199], v18 offset:2048
	ds_read_b128 v[200:203], v18 offset:4096
	ds_read_b128 v[204:207], v18 offset:6144
	ds_read_b128 v[176:179], v16 offset:2048
	ds_read_b128 v[180:183], v16 offset:4096
	ds_read_b128 v[184:187], v16 offset:6144
	s_waitcnt lgkmcnt(14)
	v_mfma_f32_16x16x32_f16 v[56:59], v[136:139], v[156:159], v[56:59]
	s_add_u32 m0, s28, 0x1e000
	s_nop 0
	global_load_lds_dwordx4 v13, s[4:5]
	s_add_u32 s4, s4, s20
	s_addc_u32 s5, s5, 0
	s_waitcnt lgkmcnt(13)
	v_mfma_f32_16x16x32_f16 v[60:63], v[136:139], v[160:163], v[60:63]
	s_waitcnt lgkmcnt(12)
	v_mfma_f32_16x16x32_f16 v[64:67], v[136:139], v[164:167], v[64:67]
	s_waitcnt lgkmcnt(11)
	v_mfma_f32_16x16x32_f16 v[68:71], v[136:139], v[168:171], v[68:71]
	s_waitcnt lgkmcnt(10)
	v_mfma_f32_16x16x32_f16 v[72:75], v[140:143], v[156:159], v[72:75]
	v_mfma_f32_16x16x32_f16 v[76:79], v[140:143], v[160:163], v[76:79]
	s_add_u32 m0, s28, 0x20000
	s_nop 0
	global_load_lds_dwordx4 v10, s[6:7]
	v_mfma_f32_16x16x32_f16 v[80:83], v[140:143], v[164:167], v[80:83]
	v_mfma_f32_16x16x32_f16 v[84:87], v[140:143], v[168:171], v[84:87]
	s_waitcnt lgkmcnt(9)
	v_mfma_f32_16x16x32_f16 v[88:91], v[144:147], v[156:159], v[88:91]
	v_mfma_f32_16x16x32_f16 v[92:95], v[144:147], v[160:163], v[92:95]
	v_mfma_f32_16x16x32_f16 v[96:99], v[144:147], v[164:167], v[96:99]
	s_add_u32 m0, s28, 0x22000
	s_nop 0
	global_load_lds_dwordx4 v11, s[6:7]
	s_add_u32 s6, s6, s20
	s_addc_u32 s7, s7, 0
	v_mfma_f32_16x16x32_f16 v[100:103], v[144:147], v[168:171], v[100:103]
	s_waitcnt lgkmcnt(8)
	v_mfma_f32_16x16x32_f16 v[104:107], v[148:151], v[156:159], v[104:107]
	v_mfma_f32_16x16x32_f16 v[108:111], v[148:151], v[160:163], v[108:111]
	v_mfma_f32_16x16x32_f16 v[112:115], v[148:151], v[164:167], v[112:115]
	v_mfma_f32_16x16x32_f16 v[116:119], v[148:151], v[168:171], v[116:119]
	s_waitcnt vmcnt(6) lgkmcnt(0)
	s_barrier
	s_waitcnt lgkmcnt(7)
	ds_read_b128 v[136:139], v15 offset:49152
	ds_read_b128 v[156:159], v17 offset:49152
	ds_read_b128 v[160:163], v17 offset:51200
	ds_read_b128 v[164:167], v17 offset:53248
	ds_read_b128 v[168:171], v17 offset:55296
	ds_read_b128 v[140:143], v15 offset:51200
	ds_read_b128 v[144:147], v15 offset:53248
	ds_read_b128 v[148:151], v15 offset:55296
	s_waitcnt lgkmcnt(14)
	v_mfma_f32_16x16x32_f16 v[56:59], v[172:175], v[192:195], v[56:59]
	s_add_u32 m0, s28, 0x0
	s_nop 0
	global_load_lds_dwordx4 v10, s[4:5]
	s_waitcnt lgkmcnt(13)
	v_mfma_f32_16x16x32_f16 v[60:63], v[172:175], v[196:199], v[60:63]
	s_waitcnt lgkmcnt(12)
	v_mfma_f32_16x16x32_f16 v[64:67], v[172:175], v[200:203], v[64:67]
	s_waitcnt lgkmcnt(11)
	v_mfma_f32_16x16x32_f16 v[68:71], v[172:175], v[204:207], v[68:71]
	s_waitcnt lgkmcnt(10)
	v_mfma_f32_16x16x32_f16 v[72:75], v[176:179], v[192:195], v[72:75]
	v_mfma_f32_16x16x32_f16 v[76:79], v[176:179], v[196:199], v[76:79]
	s_add_u32 m0, s28, 0x2000
	s_nop 0
	global_load_lds_dwordx4 v11, s[4:5]
	v_mfma_f32_16x16x32_f16 v[80:83], v[176:179], v[200:203], v[80:83]
	v_mfma_f32_16x16x32_f16 v[84:87], v[176:179], v[204:207], v[84:87]
	s_waitcnt lgkmcnt(9)
	v_mfma_f32_16x16x32_f16 v[88:91], v[180:183], v[192:195], v[88:91]
	v_mfma_f32_16x16x32_f16 v[92:95], v[180:183], v[196:199], v[92:95]
	v_mfma_f32_16x16x32_f16 v[96:99], v[180:183], v[200:203], v[96:99]
	s_add_u32 m0, s28, 0x4000
	s_nop 0
	global_load_lds_dwordx4 v12, s[4:5]
	v_mfma_f32_16x16x32_f16 v[100:103], v[180:183], v[204:207], v[100:103]
	s_waitcnt lgkmcnt(8)
	v_mfma_f32_16x16x32_f16 v[104:107], v[184:187], v[192:195], v[104:107]
	v_mfma_f32_16x16x32_f16 v[108:111], v[184:187], v[196:199], v[108:111]
	v_mfma_f32_16x16x32_f16 v[112:115], v[184:187], v[200:203], v[112:115]
	v_mfma_f32_16x16x32_f16 v[116:119], v[184:187], v[204:207], v[116:119]
	s_waitcnt lgkmcnt(7)
	ds_read_b128 v[172:175], v16 offset:49152
	ds_read_b128 v[192:195], v18 offset:49152
	ds_read_b128 v[196:199], v18 offset:51200
	ds_read_b128 v[200:203], v18 offset:53248
	ds_read_b128 v[204:207], v18 offset:55296
	ds_read_b128 v[176:179], v16 offset:51200
	ds_read_b128 v[180:183], v16 offset:53248
	ds_read_b128 v[184:187], v16 offset:55296
	s_waitcnt lgkmcnt(14)
	v_mfma_f32_16x16x32_f16 v[56:59], v[136:139], v[156:159], v[56:59]
	s_add_u32 m0, s28, 0x6000
	s_nop 0
	global_load_lds_dwordx4 v13, s[4:5]
	s_add_u32 s4, s4, s20
	s_addc_u32 s5, s5, 0
	s_waitcnt lgkmcnt(13)
	v_mfma_f32_16x16x32_f16 v[60:63], v[136:139], v[160:163], v[60:63]
	s_waitcnt lgkmcnt(12)
	v_mfma_f32_16x16x32_f16 v[64:67], v[136:139], v[164:167], v[64:67]
	s_waitcnt lgkmcnt(11)
	v_mfma_f32_16x16x32_f16 v[68:71], v[136:139], v[168:171], v[68:71]
	s_waitcnt lgkmcnt(10)
	v_mfma_f32_16x16x32_f16 v[72:75], v[140:143], v[156:159], v[72:75]
	v_mfma_f32_16x16x32_f16 v[76:79], v[140:143], v[160:163], v[76:79]
	s_add_u32 m0, s28, 0x8000
	s_nop 0
	global_load_lds_dwordx4 v10, s[6:7]
	v_mfma_f32_16x16x32_f16 v[80:83], v[140:143], v[164:167], v[80:83]
	v_mfma_f32_16x16x32_f16 v[84:87], v[140:143], v[168:171], v[84:87]
	s_waitcnt lgkmcnt(9)
	v_mfma_f32_16x16x32_f16 v[88:91], v[144:147], v[156:159], v[88:91]
	v_mfma_f32_16x16x32_f16 v[92:95], v[144:147], v[160:163], v[92:95]
	v_mfma_f32_16x16x32_f16 v[96:99], v[144:147], v[164:167], v[96:99]
	s_add_u32 m0, s28, 0xa000
	s_nop 0
	global_load_lds_dwordx4 v11, s[6:7]
	s_add_u32 s6, s6, s20
	s_addc_u32 s7, s7, 0
	v_mfma_f32_16x16x32_f16 v[100:103], v[144:147], v[168:171], v[100:103]
	s_waitcnt lgkmcnt(8)
	v_mfma_f32_16x16x32_f16 v[104:107], v[148:151], v[156:159], v[104:107]
	v_mfma_f32_16x16x32_f16 v[108:111], v[148:151], v[160:163], v[108:111]
	v_mfma_f32_16x16x32_f16 v[112:115], v[148:151], v[164:167], v[112:115]
	v_mfma_f32_16x16x32_f16 v[116:119], v[148:151], v[168:171], v[116:119]
	s_waitcnt vmcnt(6) lgkmcnt(0)
	s_barrier
	s_waitcnt lgkmcnt(7)
	ds_read_b128 v[136:139], v19
	ds_read_b128 v[156:159], v21
	ds_read_b128 v[160:163], v21 offset:2048
	ds_read_b128 v[164:167], v21 offset:4096
	ds_read_b128 v[168:171], v21 offset:6144
	ds_read_b128 v[140:143], v19 offset:2048
	ds_read_b128 v[144:147], v19 offset:4096
	ds_read_b128 v[148:151], v19 offset:6144
	s_waitcnt lgkmcnt(14)
	v_mfma_f32_16x16x32_f16 v[56:59], v[172:175], v[192:195], v[56:59]
	s_add_u32 m0, s28, 0xc000
	s_nop 0
	global_load_lds_dwordx4 v10, s[4:5]
	s_waitcnt lgkmcnt(13)
	v_mfma_f32_16x16x32_f16 v[60:63], v[172:175], v[196:199], v[60:63]
	s_waitcnt lgkmcnt(12)
	v_mfma_f32_16x16x32_f16 v[64:67], v[172:175], v[200:203], v[64:67]
	s_waitcnt lgkmcnt(11)
	v_mfma_f32_16x16x32_f16 v[68:71], v[172:175], v[204:207], v[68:71]
	s_waitcnt lgkmcnt(10)
	v_mfma_f32_16x16x32_f16 v[72:75], v[176:179], v[192:195], v[72:75]
	v_mfma_f32_16x16x32_f16 v[76:79], v[176:179], v[196:199], v[76:79]
	s_add_u32 m0, s28, 0xe000
	s_nop 0
	global_load_lds_dwordx4 v11, s[4:5]
	v_mfma_f32_16x16x32_f16 v[80:83], v[176:179], v[200:203], v[80:83]
	v_mfma_f32_16x16x32_f16 v[84:87], v[176:179], v[204:207], v[84:87]
	s_waitcnt lgkmcnt(9)
	v_mfma_f32_16x16x32_f16 v[88:91], v[180:183], v[192:195], v[88:91]
	v_mfma_f32_16x16x32_f16 v[92:95], v[180:183], v[196:199], v[92:95]
	v_mfma_f32_16x16x32_f16 v[96:99], v[180:183], v[200:203], v[96:99]
	s_add_u32 m0, s28, 0x10000
	s_nop 0
	global_load_lds_dwordx4 v12, s[4:5]
	v_mfma_f32_16x16x32_f16 v[100:103], v[180:183], v[204:207], v[100:103]
	s_waitcnt lgkmcnt(8)
	v_mfma_f32_16x16x32_f16 v[104:107], v[184:187], v[192:195], v[104:107]
	v_mfma_f32_16x16x32_f16 v[108:111], v[184:187], v[196:199], v[108:111]
	v_mfma_f32_16x16x32_f16 v[112:115], v[184:187], v[200:203], v[112:115]
	v_mfma_f32_16x16x32_f16 v[116:119], v[184:187], v[204:207], v[116:119]
	s_waitcnt lgkmcnt(7)
	ds_read_b128 v[172:175], v20
	ds_read_b128 v[192:195], v22
	ds_read_b128 v[196:199], v22 offset:2048
	ds_read_b128 v[200:203], v22 offset:4096
	ds_read_b128 v[204:207], v22 offset:6144
	ds_read_b128 v[176:179], v20 offset:2048
	ds_read_b128 v[180:183], v20 offset:4096
	ds_read_b128 v[184:187], v20 offset:6144
	s_waitcnt lgkmcnt(14)
	v_mfma_f32_16x16x32_f16 v[56:59], v[136:139], v[156:159], v[56:59]
	s_add_u32 m0, s28, 0x12000
	s_nop 0
	global_load_lds_dwordx4 v13, s[4:5]
	s_add_u32 s4, s4, s20
	s_addc_u32 s5, s5, 0
	s_waitcnt lgkmcnt(13)
	v_mfma_f32_16x16x32_f16 v[60:63], v[136:139], v[160:163], v[60:63]
	s_waitcnt lgkmcnt(12)
	v_mfma_f32_16x16x32_f16 v[64:67], v[136:139], v[164:167], v[64:67]
	s_waitcnt lgkmcnt(11)
	v_mfma_f32_16x16x32_f16 v[68:71], v[136:139], v[168:171], v[68:71]
	s_waitcnt lgkmcnt(10)
	v_mfma_f32_16x16x32_f16 v[72:75], v[140:143], v[156:159], v[72:75]
	v_mfma_f32_16x16x32_f16 v[76:79], v[140:143], v[160:163], v[76:79]
	s_add_u32 m0, s28, 0x14000
	s_nop 0
	global_load_lds_dwordx4 v10, s[6:7]
	v_mfma_f32_16x16x32_f16 v[80:83], v[140:143], v[164:167], v[80:83]
	v_mfma_f32_16x16x32_f16 v[84:87], v[140:143], v[168:171], v[84:87]
	s_waitcnt lgkmcnt(9)
	v_mfma_f32_16x16x32_f16 v[88:91], v[144:147], v[156:159], v[88:91]
	v_mfma_f32_16x16x32_f16 v[92:95], v[144:147], v[160:163], v[92:95]
	v_mfma_f32_16x16x32_f16 v[96:99], v[144:147], v[164:167], v[96:99]
	s_add_u32 m0, s28, 0x16000
	s_nop 0
	global_load_lds_dwordx4 v11, s[6:7]
	s_add_u32 s6, s6, s20
	s_addc_u32 s7, s7, 0
	v_mfma_f32_16x16x32_f16 v[100:103], v[144:147], v[168:171], v[100:103]
	s_waitcnt lgkmcnt(8)
	v_mfma_f32_16x16x32_f16 v[104:107], v[148:151], v[156:159], v[104:107]
	v_mfma_f32_16x16x32_f16 v[108:111], v[148:151], v[160:163], v[108:111]
	v_mfma_f32_16x16x32_f16 v[112:115], v[148:151], v[164:167], v[112:115]
	v_mfma_f32_16x16x32_f16 v[116:119], v[148:151], v[168:171], v[116:119]
	s_waitcnt vmcnt(6) lgkmcnt(0)
	s_barrier
	s_waitcnt lgkmcnt(7)
	ds_read_b128 v[136:139], v15
	ds_read_b128 v[156:159], v17
	ds_read_b128 v[160:163], v17 offset:2048
	ds_read_b128 v[164:167], v17 offset:4096
	ds_read_b128 v[168:171], v17 offset:6144
	ds_read_b128 v[140:143], v15 offset:2048
	ds_read_b128 v[144:147], v15 offset:4096
	ds_read_b128 v[148:151], v15 offset:6144
	s_waitcnt lgkmcnt(14)
	v_mfma_f32_16x16x32_f16 v[56:59], v[172:175], v[192:195], v[56:59]
	s_add_u32 m0, s28, 0x18000
	s_nop 0
	global_load_lds_dwordx4 v10, s[4:5]
	s_waitcnt lgkmcnt(13)
	v_mfma_f32_16x16x32_f16 v[60:63], v[172:175], v[196:199], v[60:63]
	s_waitcnt lgkmcnt(12)
	v_mfma_f32_16x16x32_f16 v[64:67], v[172:175], v[200:203], v[64:67]
	s_waitcnt lgkmcnt(11)
	v_mfma_f32_16x16x32_f16 v[68:71], v[172:175], v[204:207], v[68:71]
	s_waitcnt lgkmcnt(10)
	v_mfma_f32_16x16x32_f16 v[72:75], v[176:179], v[192:195], v[72:75]
	v_mfma_f32_16x16x32_f16 v[76:79], v[176:179], v[196:199], v[76:79]
	s_add_u32 m0, s28, 0x1a000
	s_nop 0
	global_load_lds_dwordx4 v11, s[4:5]
	v_mfma_f32_16x16x32_f16 v[80:83], v[176:179], v[200:203], v[80:83]
	v_mfma_f32_16x16x32_f16 v[84:87], v[176:179], v[204:207], v[84:87]
	s_waitcnt lgkmcnt(9)
	v_mfma_f32_16x16x32_f16 v[88:91], v[180:183], v[192:195], v[88:91]
	v_mfma_f32_16x16x32_f16 v[92:95], v[180:183], v[196:199], v[92:95]
	v_mfma_f32_16x16x32_f16 v[96:99], v[180:183], v[200:203], v[96:99]
	s_add_u32 m0, s28, 0x1c000
	s_nop 0
	global_load_lds_dwordx4 v12, s[4:5]
	v_mfma_f32_16x16x32_f16 v[100:103], v[180:183], v[204:207], v[100:103]
	s_waitcnt lgkmcnt(8)
	v_mfma_f32_16x16x32_f16 v[104:107], v[184:187], v[192:195], v[104:107]
	v_mfma_f32_16x16x32_f16 v[108:111], v[184:187], v[196:199], v[108:111]
	v_mfma_f32_16x16x32_f16 v[112:115], v[184:187], v[200:203], v[112:115]
	v_mfma_f32_16x16x32_f16 v[116:119], v[184:187], v[204:207], v[116:119]
	s_waitcnt lgkmcnt(7)
	ds_read_b128 v[172:175], v16
	ds_read_b128 v[192:195], v18
	ds_read_b128 v[196:199], v18 offset:2048
	ds_read_b128 v[200:203], v18 offset:4096
	ds_read_b128 v[204:207], v18 offset:6144
	ds_read_b128 v[176:179], v16 offset:2048
	ds_read_b128 v[180:183], v16 offset:4096
	ds_read_b128 v[184:187], v16 offset:6144
	s_waitcnt lgkmcnt(14)
	v_mfma_f32_16x16x32_f16 v[56:59], v[136:139], v[156:159], v[56:59]
	s_add_u32 m0, s28, 0x1e000
	s_nop 0
	global_load_lds_dwordx4 v13, s[4:5]
	s_add_u32 s4, s4, s20
	s_addc_u32 s5, s5, 0
	s_waitcnt lgkmcnt(13)
	v_mfma_f32_16x16x32_f16 v[60:63], v[136:139], v[160:163], v[60:63]
	s_waitcnt lgkmcnt(12)
	v_mfma_f32_16x16x32_f16 v[64:67], v[136:139], v[164:167], v[64:67]
	s_waitcnt lgkmcnt(11)
	v_mfma_f32_16x16x32_f16 v[68:71], v[136:139], v[168:171], v[68:71]
	s_waitcnt lgkmcnt(10)
	v_mfma_f32_16x16x32_f16 v[72:75], v[140:143], v[156:159], v[72:75]
	v_mfma_f32_16x16x32_f16 v[76:79], v[140:143], v[160:163], v[76:79]
	s_add_u32 m0, s28, 0x20000
	s_nop 0
	global_load_lds_dwordx4 v10, s[6:7]
	v_mfma_f32_16x16x32_f16 v[80:83], v[140:143], v[164:167], v[80:83]
	v_mfma_f32_16x16x32_f16 v[84:87], v[140:143], v[168:171], v[84:87]
	s_waitcnt lgkmcnt(9)
	v_mfma_f32_16x16x32_f16 v[88:91], v[144:147], v[156:159], v[88:91]
	v_mfma_f32_16x16x32_f16 v[92:95], v[144:147], v[160:163], v[92:95]
	v_mfma_f32_16x16x32_f16 v[96:99], v[144:147], v[164:167], v[96:99]
	s_add_u32 m0, s28, 0x22000
	s_nop 0
	global_load_lds_dwordx4 v11, s[6:7]
	s_add_u32 s6, s6, s20
	s_addc_u32 s7, s7, 0
	v_mfma_f32_16x16x32_f16 v[100:103], v[144:147], v[168:171], v[100:103]
	s_waitcnt lgkmcnt(8)
	v_mfma_f32_16x16x32_f16 v[104:107], v[148:151], v[156:159], v[104:107]
	v_mfma_f32_16x16x32_f16 v[108:111], v[148:151], v[160:163], v[108:111]
	v_mfma_f32_16x16x32_f16 v[112:115], v[148:151], v[164:167], v[112:115]
	v_mfma_f32_16x16x32_f16 v[116:119], v[148:151], v[168:171], v[116:119]
	s_waitcnt vmcnt(6) lgkmcnt(0)
	s_barrier
	s_waitcnt lgkmcnt(7)
	ds_read_b128 v[136:139], v15 offset:49152
	ds_read_b128 v[156:159], v17 offset:49152
	ds_read_b128 v[160:163], v17 offset:51200
	ds_read_b128 v[164:167], v17 offset:53248
	ds_read_b128 v[168:171], v17 offset:55296
	ds_read_b128 v[140:143], v15 offset:51200
	ds_read_b128 v[144:147], v15 offset:53248
	ds_read_b128 v[148:151], v15 offset:55296
	s_waitcnt lgkmcnt(14)
	v_mfma_f32_16x16x32_f16 v[56:59], v[172:175], v[192:195], v[56:59]
	s_add_u32 m0, s28, 0x0
	s_nop 0
	global_load_lds_dwordx4 v10, s[4:5]
	s_waitcnt lgkmcnt(13)
	v_mfma_f32_16x16x32_f16 v[60:63], v[172:175], v[196:199], v[60:63]
	s_waitcnt lgkmcnt(12)
	v_mfma_f32_16x16x32_f16 v[64:67], v[172:175], v[200:203], v[64:67]
	s_waitcnt lgkmcnt(11)
	v_mfma_f32_16x16x32_f16 v[68:71], v[172:175], v[204:207], v[68:71]
	s_waitcnt lgkmcnt(10)
	v_mfma_f32_16x16x32_f16 v[72:75], v[176:179], v[192:195], v[72:75]
	v_mfma_f32_16x16x32_f16 v[76:79], v[176:179], v[196:199], v[76:79]
	s_add_u32 m0, s28, 0x2000
	s_nop 0
	global_load_lds_dwordx4 v11, s[4:5]
	v_mfma_f32_16x16x32_f16 v[80:83], v[176:179], v[200:203], v[80:83]
	v_mfma_f32_16x16x32_f16 v[84:87], v[176:179], v[204:207], v[84:87]
	s_waitcnt lgkmcnt(9)
	v_mfma_f32_16x16x32_f16 v[88:91], v[180:183], v[192:195], v[88:91]
	v_mfma_f32_16x16x32_f16 v[92:95], v[180:183], v[196:199], v[92:95]
	v_mfma_f32_16x16x32_f16 v[96:99], v[180:183], v[200:203], v[96:99]
	s_add_u32 m0, s28, 0x4000
	s_nop 0
	global_load_lds_dwordx4 v12, s[4:5]
	v_mfma_f32_16x16x32_f16 v[100:103], v[180:183], v[204:207], v[100:103]
	s_waitcnt lgkmcnt(8)
	v_mfma_f32_16x16x32_f16 v[104:107], v[184:187], v[192:195], v[104:107]
	v_mfma_f32_16x16x32_f16 v[108:111], v[184:187], v[196:199], v[108:111]
	v_mfma_f32_16x16x32_f16 v[112:115], v[184:187], v[200:203], v[112:115]
	v_mfma_f32_16x16x32_f16 v[116:119], v[184:187], v[204:207], v[116:119]
	s_waitcnt lgkmcnt(7)
	ds_read_b128 v[172:175], v16 offset:49152
	ds_read_b128 v[192:195], v18 offset:49152
	ds_read_b128 v[196:199], v18 offset:51200
	ds_read_b128 v[200:203], v18 offset:53248
	ds_read_b128 v[204:207], v18 offset:55296
	ds_read_b128 v[176:179], v16 offset:51200
	ds_read_b128 v[180:183], v16 offset:53248
	ds_read_b128 v[184:187], v16 offset:55296
	s_waitcnt lgkmcnt(14)
	v_mfma_f32_16x16x32_f16 v[56:59], v[136:139], v[156:159], v[56:59]
	s_add_u32 m0, s28, 0x6000
	s_nop 0
	global_load_lds_dwordx4 v13, s[4:5]
	s_add_u32 s4, s4, s20
	s_addc_u32 s5, s5, 0
	s_waitcnt lgkmcnt(13)
	v_mfma_f32_16x16x32_f16 v[60:63], v[136:139], v[160:163], v[60:63]
	s_waitcnt lgkmcnt(12)
	v_mfma_f32_16x16x32_f16 v[64:67], v[136:139], v[164:167], v[64:67]
	s_waitcnt lgkmcnt(11)
	v_mfma_f32_16x16x32_f16 v[68:71], v[136:139], v[168:171], v[68:71]
	s_waitcnt lgkmcnt(10)
	v_mfma_f32_16x16x32_f16 v[72:75], v[140:143], v[156:159], v[72:75]
	v_mfma_f32_16x16x32_f16 v[76:79], v[140:143], v[160:163], v[76:79]
	s_add_u32 m0, s28, 0x8000
	s_nop 0
	global_load_lds_dwordx4 v10, s[6:7]
	v_mfma_f32_16x16x32_f16 v[80:83], v[140:143], v[164:167], v[80:83]
	v_mfma_f32_16x16x32_f16 v[84:87], v[140:143], v[168:171], v[84:87]
	s_waitcnt lgkmcnt(9)
	v_mfma_f32_16x16x32_f16 v[88:91], v[144:147], v[156:159], v[88:91]
	v_mfma_f32_16x16x32_f16 v[92:95], v[144:147], v[160:163], v[92:95]
	v_mfma_f32_16x16x32_f16 v[96:99], v[144:147], v[164:167], v[96:99]
	s_add_u32 m0, s28, 0xa000
	s_nop 0
	global_load_lds_dwordx4 v11, s[6:7]
	s_add_u32 s6, s6, s20
	s_addc_u32 s7, s7, 0
	v_mfma_f32_16x16x32_f16 v[100:103], v[144:147], v[168:171], v[100:103]
	s_waitcnt lgkmcnt(8)
	v_mfma_f32_16x16x32_f16 v[104:107], v[148:151], v[156:159], v[104:107]
	v_mfma_f32_16x16x32_f16 v[108:111], v[148:151], v[160:163], v[108:111]
	v_mfma_f32_16x16x32_f16 v[112:115], v[148:151], v[164:167], v[112:115]
	v_mfma_f32_16x16x32_f16 v[116:119], v[148:151], v[168:171], v[116:119]
	s_waitcnt vmcnt(6) lgkmcnt(0)
	s_barrier
	s_waitcnt lgkmcnt(7)
	ds_read_b128 v[136:139], v19
	ds_read_b128 v[156:159], v21
	ds_read_b128 v[160:163], v21 offset:2048
	ds_read_b128 v[164:167], v21 offset:4096
	ds_read_b128 v[168:171], v21 offset:6144
	ds_read_b128 v[140:143], v19 offset:2048
	ds_read_b128 v[144:147], v19 offset:4096
	ds_read_b128 v[148:151], v19 offset:6144
	s_waitcnt lgkmcnt(14)
	v_mfma_f32_16x16x32_f16 v[56:59], v[172:175], v[192:195], v[56:59]
	s_add_u32 m0, s28, 0xc000
	s_nop 0
	global_load_lds_dwordx4 v10, s[4:5]
	s_waitcnt lgkmcnt(13)
	v_mfma_f32_16x16x32_f16 v[60:63], v[172:175], v[196:199], v[60:63]
	s_waitcnt lgkmcnt(12)
	v_mfma_f32_16x16x32_f16 v[64:67], v[172:175], v[200:203], v[64:67]
	s_waitcnt lgkmcnt(11)
	v_mfma_f32_16x16x32_f16 v[68:71], v[172:175], v[204:207], v[68:71]
	s_waitcnt lgkmcnt(10)
	v_mfma_f32_16x16x32_f16 v[72:75], v[176:179], v[192:195], v[72:75]
	v_mfma_f32_16x16x32_f16 v[76:79], v[176:179], v[196:199], v[76:79]
	s_add_u32 m0, s28, 0xe000
	s_nop 0
	global_load_lds_dwordx4 v11, s[4:5]
	v_mfma_f32_16x16x32_f16 v[80:83], v[176:179], v[200:203], v[80:83]
	v_mfma_f32_16x16x32_f16 v[84:87], v[176:179], v[204:207], v[84:87]
	s_waitcnt lgkmcnt(9)
	v_mfma_f32_16x16x32_f16 v[88:91], v[180:183], v[192:195], v[88:91]
	v_mfma_f32_16x16x32_f16 v[92:95], v[180:183], v[196:199], v[92:95]
	v_mfma_f32_16x16x32_f16 v[96:99], v[180:183], v[200:203], v[96:99]
	s_add_u32 m0, s28, 0x10000
	s_nop 0
	global_load_lds_dwordx4 v12, s[4:5]
	v_mfma_f32_16x16x32_f16 v[100:103], v[180:183], v[204:207], v[100:103]
	s_waitcnt lgkmcnt(8)
	v_mfma_f32_16x16x32_f16 v[104:107], v[184:187], v[192:195], v[104:107]
	v_mfma_f32_16x16x32_f16 v[108:111], v[184:187], v[196:199], v[108:111]
	v_mfma_f32_16x16x32_f16 v[112:115], v[184:187], v[200:203], v[112:115]
	v_mfma_f32_16x16x32_f16 v[116:119], v[184:187], v[204:207], v[116:119]
	s_waitcnt lgkmcnt(7)
	ds_read_b128 v[172:175], v20
	ds_read_b128 v[192:195], v22
	ds_read_b128 v[196:199], v22 offset:2048
	ds_read_b128 v[200:203], v22 offset:4096
	ds_read_b128 v[204:207], v22 offset:6144
	ds_read_b128 v[176:179], v20 offset:2048
	ds_read_b128 v[180:183], v20 offset:4096
	ds_read_b128 v[184:187], v20 offset:6144
	s_waitcnt lgkmcnt(14)
	v_mfma_f32_16x16x32_f16 v[56:59], v[136:139], v[156:159], v[56:59]
	s_add_u32 m0, s28, 0x12000
	s_nop 0
	global_load_lds_dwordx4 v13, s[4:5]
	s_add_u32 s4, s4, s20
	s_addc_u32 s5, s5, 0
	s_waitcnt lgkmcnt(13)
	v_mfma_f32_16x16x32_f16 v[60:63], v[136:139], v[160:163], v[60:63]
	s_waitcnt lgkmcnt(12)
	v_mfma_f32_16x16x32_f16 v[64:67], v[136:139], v[164:167], v[64:67]
	s_waitcnt lgkmcnt(11)
	v_mfma_f32_16x16x32_f16 v[68:71], v[136:139], v[168:171], v[68:71]
	s_waitcnt lgkmcnt(10)
	v_mfma_f32_16x16x32_f16 v[72:75], v[140:143], v[156:159], v[72:75]
	v_mfma_f32_16x16x32_f16 v[76:79], v[140:143], v[160:163], v[76:79]
	s_add_u32 m0, s28, 0x14000
	s_nop 0
	global_load_lds_dwordx4 v10, s[6:7]
	v_mfma_f32_16x16x32_f16 v[80:83], v[140:143], v[164:167], v[80:83]
	v_mfma_f32_16x16x32_f16 v[84:87], v[140:143], v[168:171], v[84:87]
	s_waitcnt lgkmcnt(9)
	v_mfma_f32_16x16x32_f16 v[88:91], v[144:147], v[156:159], v[88:91]
	v_mfma_f32_16x16x32_f16 v[92:95], v[144:147], v[160:163], v[92:95]
	v_mfma_f32_16x16x32_f16 v[96:99], v[144:147], v[164:167], v[96:99]
	s_add_u32 m0, s28, 0x16000
	s_nop 0
	global_load_lds_dwordx4 v11, s[6:7]
	s_add_u32 s6, s6, s20
	s_addc_u32 s7, s7, 0
	v_mfma_f32_16x16x32_f16 v[100:103], v[144:147], v[168:171], v[100:103]
	s_waitcnt lgkmcnt(8)
	v_mfma_f32_16x16x32_f16 v[104:107], v[148:151], v[156:159], v[104:107]
	v_mfma_f32_16x16x32_f16 v[108:111], v[148:151], v[160:163], v[108:111]
	v_mfma_f32_16x16x32_f16 v[112:115], v[148:151], v[164:167], v[112:115]
	v_mfma_f32_16x16x32_f16 v[116:119], v[148:151], v[168:171], v[116:119]
	s_waitcnt vmcnt(6) lgkmcnt(0)
	s_barrier
	s_waitcnt lgkmcnt(7)
	ds_read_b128 v[136:139], v15
	ds_read_b128 v[156:159], v17
	ds_read_b128 v[160:163], v17 offset:2048
	ds_read_b128 v[164:167], v17 offset:4096
	ds_read_b128 v[168:171], v17 offset:6144
	ds_read_b128 v[140:143], v15 offset:2048
	ds_read_b128 v[144:147], v15 offset:4096
	ds_read_b128 v[148:151], v15 offset:6144
	s_waitcnt lgkmcnt(14)
	v_mfma_f32_16x16x32_f16 v[56:59], v[172:175], v[192:195], v[56:59]
	s_add_u32 m0, s28, 0x18000
	s_nop 0
	global_load_lds_dwordx4 v10, s[4:5]
	s_waitcnt lgkmcnt(13)
	v_mfma_f32_16x16x32_f16 v[60:63], v[172:175], v[196:199], v[60:63]
	s_waitcnt lgkmcnt(12)
	v_mfma_f32_16x16x32_f16 v[64:67], v[172:175], v[200:203], v[64:67]
	s_waitcnt lgkmcnt(11)
	v_mfma_f32_16x16x32_f16 v[68:71], v[172:175], v[204:207], v[68:71]
	s_waitcnt lgkmcnt(10)
	v_mfma_f32_16x16x32_f16 v[72:75], v[176:179], v[192:195], v[72:75]
	v_mfma_f32_16x16x32_f16 v[76:79], v[176:179], v[196:199], v[76:79]
	s_add_u32 m0, s28, 0x1a000
	s_nop 0
	global_load_lds_dwordx4 v11, s[4:5]
	v_mfma_f32_16x16x32_f16 v[80:83], v[176:179], v[200:203], v[80:83]
	v_mfma_f32_16x16x32_f16 v[84:87], v[176:179], v[204:207], v[84:87]
	s_waitcnt lgkmcnt(9)
	v_mfma_f32_16x16x32_f16 v[88:91], v[180:183], v[192:195], v[88:91]
	v_mfma_f32_16x16x32_f16 v[92:95], v[180:183], v[196:199], v[92:95]
	v_mfma_f32_16x16x32_f16 v[96:99], v[180:183], v[200:203], v[96:99]
	s_add_u32 m0, s28, 0x1c000
	s_nop 0
	global_load_lds_dwordx4 v12, s[4:5]
	v_mfma_f32_16x16x32_f16 v[100:103], v[180:183], v[204:207], v[100:103]
	s_waitcnt lgkmcnt(8)
	v_mfma_f32_16x16x32_f16 v[104:107], v[184:187], v[192:195], v[104:107]
	v_mfma_f32_16x16x32_f16 v[108:111], v[184:187], v[196:199], v[108:111]
	v_mfma_f32_16x16x32_f16 v[112:115], v[184:187], v[200:203], v[112:115]
	v_mfma_f32_16x16x32_f16 v[116:119], v[184:187], v[204:207], v[116:119]
	s_waitcnt lgkmcnt(7)
	ds_read_b128 v[172:175], v16
	ds_read_b128 v[192:195], v18
	ds_read_b128 v[196:199], v18 offset:2048
	ds_read_b128 v[200:203], v18 offset:4096
	ds_read_b128 v[204:207], v18 offset:6144
	ds_read_b128 v[176:179], v16 offset:2048
	ds_read_b128 v[180:183], v16 offset:4096
	ds_read_b128 v[184:187], v16 offset:6144
	s_waitcnt lgkmcnt(14)
	v_mfma_f32_16x16x32_f16 v[56:59], v[136:139], v[156:159], v[56:59]
	s_add_u32 m0, s28, 0x1e000
	s_nop 0
	global_load_lds_dwordx4 v13, s[4:5]
	s_add_u32 s4, s4, s20
	s_addc_u32 s5, s5, 0
	s_waitcnt lgkmcnt(13)
	v_mfma_f32_16x16x32_f16 v[60:63], v[136:139], v[160:163], v[60:63]
	s_waitcnt lgkmcnt(12)
	v_mfma_f32_16x16x32_f16 v[64:67], v[136:139], v[164:167], v[64:67]
	s_waitcnt lgkmcnt(11)
	v_mfma_f32_16x16x32_f16 v[68:71], v[136:139], v[168:171], v[68:71]
	s_waitcnt lgkmcnt(10)
	v_mfma_f32_16x16x32_f16 v[72:75], v[140:143], v[156:159], v[72:75]
	v_mfma_f32_16x16x32_f16 v[76:79], v[140:143], v[160:163], v[76:79]
	s_add_u32 m0, s28, 0x20000
	s_nop 0
	global_load_lds_dwordx4 v10, s[6:7]
	v_mfma_f32_16x16x32_f16 v[80:83], v[140:143], v[164:167], v[80:83]
	v_mfma_f32_16x16x32_f16 v[84:87], v[140:143], v[168:171], v[84:87]
	s_waitcnt lgkmcnt(9)
	v_mfma_f32_16x16x32_f16 v[88:91], v[144:147], v[156:159], v[88:91]
	v_mfma_f32_16x16x32_f16 v[92:95], v[144:147], v[160:163], v[92:95]
	v_mfma_f32_16x16x32_f16 v[96:99], v[144:147], v[164:167], v[96:99]
	s_add_u32 m0, s28, 0x22000
	s_nop 0
	global_load_lds_dwordx4 v11, s[6:7]
	s_add_u32 s6, s6, s20
	s_addc_u32 s7, s7, 0
	v_mfma_f32_16x16x32_f16 v[100:103], v[144:147], v[168:171], v[100:103]
	s_waitcnt lgkmcnt(8)
	v_mfma_f32_16x16x32_f16 v[104:107], v[148:151], v[156:159], v[104:107]
	v_mfma_f32_16x16x32_f16 v[108:111], v[148:151], v[160:163], v[108:111]
	v_mfma_f32_16x16x32_f16 v[112:115], v[148:151], v[164:167], v[112:115]
	v_mfma_f32_16x16x32_f16 v[116:119], v[148:151], v[168:171], v[116:119]
	s_waitcnt vmcnt(6) lgkmcnt(0)
	s_barrier
	s_waitcnt lgkmcnt(7)
	ds_read_b128 v[136:139], v15 offset:49152
	ds_read_b128 v[156:159], v17 offset:49152
	ds_read_b128 v[160:163], v17 offset:51200
	ds_read_b128 v[164:167], v17 offset:53248
	ds_read_b128 v[168:171], v17 offset:55296
	ds_read_b128 v[140:143], v15 offset:51200
	ds_read_b128 v[144:147], v15 offset:53248
	ds_read_b128 v[148:151], v15 offset:55296
	s_waitcnt lgkmcnt(14)
	v_mfma_f32_16x16x32_f16 v[56:59], v[172:175], v[192:195], v[56:59]
	s_add_u32 m0, s28, 0x0
	s_nop 0
	global_load_lds_dwordx4 v10, s[4:5]
	s_waitcnt lgkmcnt(13)
	v_mfma_f32_16x16x32_f16 v[60:63], v[172:175], v[196:199], v[60:63]
	s_waitcnt lgkmcnt(12)
	v_mfma_f32_16x16x32_f16 v[64:67], v[172:175], v[200:203], v[64:67]
	s_waitcnt lgkmcnt(11)
	v_mfma_f32_16x16x32_f16 v[68:71], v[172:175], v[204:207], v[68:71]
	s_waitcnt lgkmcnt(10)
	v_mfma_f32_16x16x32_f16 v[72:75], v[176:179], v[192:195], v[72:75]
	v_mfma_f32_16x16x32_f16 v[76:79], v[176:179], v[196:199], v[76:79]
	s_add_u32 m0, s28, 0x2000
	s_nop 0
	global_load_lds_dwordx4 v11, s[4:5]
	v_mfma_f32_16x16x32_f16 v[80:83], v[176:179], v[200:203], v[80:83]
	v_mfma_f32_16x16x32_f16 v[84:87], v[176:179], v[204:207], v[84:87]
	s_waitcnt lgkmcnt(9)
	v_mfma_f32_16x16x32_f16 v[88:91], v[180:183], v[192:195], v[88:91]
	v_mfma_f32_16x16x32_f16 v[92:95], v[180:183], v[196:199], v[92:95]
	v_mfma_f32_16x16x32_f16 v[96:99], v[180:183], v[200:203], v[96:99]
	s_add_u32 m0, s28, 0x4000
	s_nop 0
	global_load_lds_dwordx4 v12, s[4:5]
	v_mfma_f32_16x16x32_f16 v[100:103], v[180:183], v[204:207], v[100:103]
	s_waitcnt lgkmcnt(8)
	v_mfma_f32_16x16x32_f16 v[104:107], v[184:187], v[192:195], v[104:107]
	v_mfma_f32_16x16x32_f16 v[108:111], v[184:187], v[196:199], v[108:111]
	v_mfma_f32_16x16x32_f16 v[112:115], v[184:187], v[200:203], v[112:115]
	v_mfma_f32_16x16x32_f16 v[116:119], v[184:187], v[204:207], v[116:119]
	s_waitcnt lgkmcnt(7)
	ds_read_b128 v[172:175], v16 offset:49152
	ds_read_b128 v[192:195], v18 offset:49152
	ds_read_b128 v[196:199], v18 offset:51200
	ds_read_b128 v[200:203], v18 offset:53248
	ds_read_b128 v[204:207], v18 offset:55296
	ds_read_b128 v[176:179], v16 offset:51200
	ds_read_b128 v[180:183], v16 offset:53248
	ds_read_b128 v[184:187], v16 offset:55296
	s_waitcnt lgkmcnt(14)
	v_mfma_f32_16x16x32_f16 v[56:59], v[136:139], v[156:159], v[56:59]
	s_add_u32 m0, s28, 0x6000
	s_nop 0
	global_load_lds_dwordx4 v13, s[4:5]
	s_add_u32 s4, s4, s20
	s_addc_u32 s5, s5, 0
	s_waitcnt lgkmcnt(13)
	v_mfma_f32_16x16x32_f16 v[60:63], v[136:139], v[160:163], v[60:63]
	s_waitcnt lgkmcnt(12)
	v_mfma_f32_16x16x32_f16 v[64:67], v[136:139], v[164:167], v[64:67]
	s_waitcnt lgkmcnt(11)
	v_mfma_f32_16x16x32_f16 v[68:71], v[136:139], v[168:171], v[68:71]
	s_waitcnt lgkmcnt(10)
	v_mfma_f32_16x16x32_f16 v[72:75], v[140:143], v[156:159], v[72:75]
	v_mfma_f32_16x16x32_f16 v[76:79], v[140:143], v[160:163], v[76:79]
	s_add_u32 m0, s28, 0x8000
	s_nop 0
	global_load_lds_dwordx4 v10, s[6:7]
	v_mfma_f32_16x16x32_f16 v[80:83], v[140:143], v[164:167], v[80:83]
	v_mfma_f32_16x16x32_f16 v[84:87], v[140:143], v[168:171], v[84:87]
	s_waitcnt lgkmcnt(9)
	v_mfma_f32_16x16x32_f16 v[88:91], v[144:147], v[156:159], v[88:91]
	v_mfma_f32_16x16x32_f16 v[92:95], v[144:147], v[160:163], v[92:95]
	v_mfma_f32_16x16x32_f16 v[96:99], v[144:147], v[164:167], v[96:99]
	s_add_u32 m0, s28, 0xa000
	s_nop 0
	global_load_lds_dwordx4 v11, s[6:7]
	s_add_u32 s6, s6, s20
	s_addc_u32 s7, s7, 0
	v_mfma_f32_16x16x32_f16 v[100:103], v[144:147], v[168:171], v[100:103]
	s_waitcnt lgkmcnt(8)
	v_mfma_f32_16x16x32_f16 v[104:107], v[148:151], v[156:159], v[104:107]
	v_mfma_f32_16x16x32_f16 v[108:111], v[148:151], v[160:163], v[108:111]
	v_mfma_f32_16x16x32_f16 v[112:115], v[148:151], v[164:167], v[112:115]
	v_mfma_f32_16x16x32_f16 v[116:119], v[148:151], v[168:171], v[116:119]
	s_waitcnt vmcnt(6) lgkmcnt(0)
	s_barrier
	s_waitcnt lgkmcnt(7)
	ds_read_b128 v[136:139], v19
	ds_read_b128 v[156:159], v21
	ds_read_b128 v[160:163], v21 offset:2048
	ds_read_b128 v[164:167], v21 offset:4096
	ds_read_b128 v[168:171], v21 offset:6144
	ds_read_b128 v[140:143], v19 offset:2048
	ds_read_b128 v[144:147], v19 offset:4096
	ds_read_b128 v[148:151], v19 offset:6144
	s_waitcnt lgkmcnt(14)
	v_mfma_f32_16x16x32_f16 v[56:59], v[172:175], v[192:195], v[56:59]
	s_add_u32 m0, s28, 0xc000
	s_nop 0
	global_load_lds_dwordx4 v10, s[4:5]
	s_waitcnt lgkmcnt(13)
	v_mfma_f32_16x16x32_f16 v[60:63], v[172:175], v[196:199], v[60:63]
	s_waitcnt lgkmcnt(12)
	v_mfma_f32_16x16x32_f16 v[64:67], v[172:175], v[200:203], v[64:67]
	s_waitcnt lgkmcnt(11)
	v_mfma_f32_16x16x32_f16 v[68:71], v[172:175], v[204:207], v[68:71]
	s_waitcnt lgkmcnt(10)
	v_mfma_f32_16x16x32_f16 v[72:75], v[176:179], v[192:195], v[72:75]
	v_mfma_f32_16x16x32_f16 v[76:79], v[176:179], v[196:199], v[76:79]
	s_add_u32 m0, s28, 0xe000
	s_nop 0
	global_load_lds_dwordx4 v11, s[4:5]
	v_mfma_f32_16x16x32_f16 v[80:83], v[176:179], v[200:203], v[80:83]
	v_mfma_f32_16x16x32_f16 v[84:87], v[176:179], v[204:207], v[84:87]
	s_waitcnt lgkmcnt(9)
	v_mfma_f32_16x16x32_f16 v[88:91], v[180:183], v[192:195], v[88:91]
	v_mfma_f32_16x16x32_f16 v[92:95], v[180:183], v[196:199], v[92:95]
	v_mfma_f32_16x16x32_f16 v[96:99], v[180:183], v[200:203], v[96:99]
	s_add_u32 m0, s28, 0x10000
	s_nop 0
	global_load_lds_dwordx4 v12, s[4:5]
	v_mfma_f32_16x16x32_f16 v[100:103], v[180:183], v[204:207], v[100:103]
	s_waitcnt lgkmcnt(8)
	v_mfma_f32_16x16x32_f16 v[104:107], v[184:187], v[192:195], v[104:107]
	v_mfma_f32_16x16x32_f16 v[108:111], v[184:187], v[196:199], v[108:111]
	v_mfma_f32_16x16x32_f16 v[112:115], v[184:187], v[200:203], v[112:115]
	v_mfma_f32_16x16x32_f16 v[116:119], v[184:187], v[204:207], v[116:119]
	s_waitcnt lgkmcnt(7)
	ds_read_b128 v[172:175], v20
	ds_read_b128 v[192:195], v22
	ds_read_b128 v[196:199], v22 offset:2048
	ds_read_b128 v[200:203], v22 offset:4096
	ds_read_b128 v[204:207], v22 offset:6144
	ds_read_b128 v[176:179], v20 offset:2048
	ds_read_b128 v[180:183], v20 offset:4096
	ds_read_b128 v[184:187], v20 offset:6144
	s_waitcnt lgkmcnt(14)
	v_mfma_f32_16x16x32_f16 v[56:59], v[136:139], v[156:159], v[56:59]
	s_add_u32 m0, s28, 0x12000
	s_nop 0
	global_load_lds_dwordx4 v13, s[4:5]
	s_add_u32 s4, s4, s20
	s_addc_u32 s5, s5, 0
	s_waitcnt lgkmcnt(13)
	v_mfma_f32_16x16x32_f16 v[60:63], v[136:139], v[160:163], v[60:63]
	s_waitcnt lgkmcnt(12)
	v_mfma_f32_16x16x32_f16 v[64:67], v[136:139], v[164:167], v[64:67]
	s_waitcnt lgkmcnt(11)
	v_mfma_f32_16x16x32_f16 v[68:71], v[136:139], v[168:171], v[68:71]
	s_waitcnt lgkmcnt(10)
	v_mfma_f32_16x16x32_f16 v[72:75], v[140:143], v[156:159], v[72:75]
	v_mfma_f32_16x16x32_f16 v[76:79], v[140:143], v[160:163], v[76:79]
	s_add_u32 m0, s28, 0x14000
	s_nop 0
	global_load_lds_dwordx4 v10, s[6:7]
	v_mfma_f32_16x16x32_f16 v[80:83], v[140:143], v[164:167], v[80:83]
	v_mfma_f32_16x16x32_f16 v[84:87], v[140:143], v[168:171], v[84:87]
	s_waitcnt lgkmcnt(9)
	v_mfma_f32_16x16x32_f16 v[88:91], v[144:147], v[156:159], v[88:91]
	v_mfma_f32_16x16x32_f16 v[92:95], v[144:147], v[160:163], v[92:95]
	v_mfma_f32_16x16x32_f16 v[96:99], v[144:147], v[164:167], v[96:99]
	s_add_u32 m0, s28, 0x16000
	s_nop 0
	global_load_lds_dwordx4 v11, s[6:7]
	s_add_u32 s6, s6, s20
	s_addc_u32 s7, s7, 0
	v_mfma_f32_16x16x32_f16 v[100:103], v[144:147], v[168:171], v[100:103]
	s_waitcnt lgkmcnt(8)
	v_mfma_f32_16x16x32_f16 v[104:107], v[148:151], v[156:159], v[104:107]
	v_mfma_f32_16x16x32_f16 v[108:111], v[148:151], v[160:163], v[108:111]
	v_mfma_f32_16x16x32_f16 v[112:115], v[148:151], v[164:167], v[112:115]
	v_mfma_f32_16x16x32_f16 v[116:119], v[148:151], v[168:171], v[116:119]
	s_waitcnt vmcnt(6) lgkmcnt(0)
	s_barrier
	s_waitcnt lgkmcnt(7)
	ds_read_b128 v[136:139], v15
	ds_read_b128 v[156:159], v17
	ds_read_b128 v[160:163], v17 offset:2048
	ds_read_b128 v[164:167], v17 offset:4096
	ds_read_b128 v[168:171], v17 offset:6144
	ds_read_b128 v[140:143], v15 offset:2048
	ds_read_b128 v[144:147], v15 offset:4096
	ds_read_b128 v[148:151], v15 offset:6144
	s_waitcnt lgkmcnt(14)
	v_mfma_f32_16x16x32_f16 v[56:59], v[172:175], v[192:195], v[56:59]
	s_add_u32 m0, s28, 0x18000
	s_nop 0
	global_load_lds_dwordx4 v10, s[4:5]
	s_waitcnt lgkmcnt(13)
	v_mfma_f32_16x16x32_f16 v[60:63], v[172:175], v[196:199], v[60:63]
	s_waitcnt lgkmcnt(12)
	v_mfma_f32_16x16x32_f16 v[64:67], v[172:175], v[200:203], v[64:67]
	s_waitcnt lgkmcnt(11)
	v_mfma_f32_16x16x32_f16 v[68:71], v[172:175], v[204:207], v[68:71]
	s_waitcnt lgkmcnt(10)
	v_mfma_f32_16x16x32_f16 v[72:75], v[176:179], v[192:195], v[72:75]
	v_mfma_f32_16x16x32_f16 v[76:79], v[176:179], v[196:199], v[76:79]
	s_add_u32 m0, s28, 0x1a000
	s_nop 0
	global_load_lds_dwordx4 v11, s[4:5]
	v_mfma_f32_16x16x32_f16 v[80:83], v[176:179], v[200:203], v[80:83]
	v_mfma_f32_16x16x32_f16 v[84:87], v[176:179], v[204:207], v[84:87]
	s_waitcnt lgkmcnt(9)
	v_mfma_f32_16x16x32_f16 v[88:91], v[180:183], v[192:195], v[88:91]
	v_mfma_f32_16x16x32_f16 v[92:95], v[180:183], v[196:199], v[92:95]
	v_mfma_f32_16x16x32_f16 v[96:99], v[180:183], v[200:203], v[96:99]
	s_add_u32 m0, s28, 0x1c000
	s_nop 0
	global_load_lds_dwordx4 v12, s[4:5]
	v_mfma_f32_16x16x32_f16 v[100:103], v[180:183], v[204:207], v[100:103]
	s_waitcnt lgkmcnt(8)
	v_mfma_f32_16x16x32_f16 v[104:107], v[184:187], v[192:195], v[104:107]
	v_mfma_f32_16x16x32_f16 v[108:111], v[184:187], v[196:199], v[108:111]
	v_mfma_f32_16x16x32_f16 v[112:115], v[184:187], v[200:203], v[112:115]
	v_mfma_f32_16x16x32_f16 v[116:119], v[184:187], v[204:207], v[116:119]
	s_waitcnt lgkmcnt(7)
	ds_read_b128 v[172:175], v16
	ds_read_b128 v[192:195], v18
	ds_read_b128 v[196:199], v18 offset:2048
	ds_read_b128 v[200:203], v18 offset:4096
	ds_read_b128 v[204:207], v18 offset:6144
	ds_read_b128 v[176:179], v16 offset:2048
	ds_read_b128 v[180:183], v16 offset:4096
	ds_read_b128 v[184:187], v16 offset:6144
	s_waitcnt lgkmcnt(14)
	v_mfma_f32_16x16x32_f16 v[56:59], v[136:139], v[156:159], v[56:59]
	s_add_u32 m0, s28, 0x1e000
	s_nop 0
	global_load_lds_dwordx4 v13, s[4:5]
	s_add_u32 s4, s4, s20
	s_addc_u32 s5, s5, 0
	s_waitcnt lgkmcnt(13)
	v_mfma_f32_16x16x32_f16 v[60:63], v[136:139], v[160:163], v[60:63]
	s_waitcnt lgkmcnt(12)
	v_mfma_f32_16x16x32_f16 v[64:67], v[136:139], v[164:167], v[64:67]
	s_waitcnt lgkmcnt(11)
	v_mfma_f32_16x16x32_f16 v[68:71], v[136:139], v[168:171], v[68:71]
	s_waitcnt lgkmcnt(10)
	v_mfma_f32_16x16x32_f16 v[72:75], v[140:143], v[156:159], v[72:75]
	v_mfma_f32_16x16x32_f16 v[76:79], v[140:143], v[160:163], v[76:79]
	s_add_u32 m0, s28, 0x20000
	s_nop 0
	global_load_lds_dwordx4 v10, s[6:7]
	v_mfma_f32_16x16x32_f16 v[80:83], v[140:143], v[164:167], v[80:83]
	v_mfma_f32_16x16x32_f16 v[84:87], v[140:143], v[168:171], v[84:87]
	s_waitcnt lgkmcnt(9)
	v_mfma_f32_16x16x32_f16 v[88:91], v[144:147], v[156:159], v[88:91]
	v_mfma_f32_16x16x32_f16 v[92:95], v[144:147], v[160:163], v[92:95]
	v_mfma_f32_16x16x32_f16 v[96:99], v[144:147], v[164:167], v[96:99]
	s_add_u32 m0, s28, 0x22000
	s_nop 0
	global_load_lds_dwordx4 v11, s[6:7]
	s_add_u32 s6, s6, s20
	s_addc_u32 s7, s7, 0
	v_mfma_f32_16x16x32_f16 v[100:103], v[144:147], v[168:171], v[100:103]
	s_waitcnt lgkmcnt(8)
	v_mfma_f32_16x16x32_f16 v[104:107], v[148:151], v[156:159], v[104:107]
	v_mfma_f32_16x16x32_f16 v[108:111], v[148:151], v[160:163], v[108:111]
	v_mfma_f32_16x16x32_f16 v[112:115], v[148:151], v[164:167], v[112:115]
	v_mfma_f32_16x16x32_f16 v[116:119], v[148:151], v[168:171], v[116:119]
	s_waitcnt vmcnt(6) lgkmcnt(0)
	s_barrier
	s_waitcnt lgkmcnt(7)
	ds_read_b128 v[136:139], v15 offset:49152
	ds_read_b128 v[156:159], v17 offset:49152
	ds_read_b128 v[160:163], v17 offset:51200
	ds_read_b128 v[164:167], v17 offset:53248
	ds_read_b128 v[168:171], v17 offset:55296
	ds_read_b128 v[140:143], v15 offset:51200
	ds_read_b128 v[144:147], v15 offset:53248
	ds_read_b128 v[148:151], v15 offset:55296
	s_waitcnt lgkmcnt(14)
	v_mfma_f32_16x16x32_f16 v[56:59], v[172:175], v[192:195], v[56:59]
	s_add_u32 m0, s28, 0x0
	s_nop 0
	global_load_lds_dwordx4 v10, s[4:5]
	s_waitcnt lgkmcnt(13)
	v_mfma_f32_16x16x32_f16 v[60:63], v[172:175], v[196:199], v[60:63]
	s_waitcnt lgkmcnt(12)
	v_mfma_f32_16x16x32_f16 v[64:67], v[172:175], v[200:203], v[64:67]
	s_waitcnt lgkmcnt(11)
	v_mfma_f32_16x16x32_f16 v[68:71], v[172:175], v[204:207], v[68:71]
	s_waitcnt lgkmcnt(10)
	v_mfma_f32_16x16x32_f16 v[72:75], v[176:179], v[192:195], v[72:75]
	v_mfma_f32_16x16x32_f16 v[76:79], v[176:179], v[196:199], v[76:79]
	s_add_u32 m0, s28, 0x2000
	s_nop 0
	global_load_lds_dwordx4 v11, s[4:5]
	v_mfma_f32_16x16x32_f16 v[80:83], v[176:179], v[200:203], v[80:83]
	v_mfma_f32_16x16x32_f16 v[84:87], v[176:179], v[204:207], v[84:87]
	s_waitcnt lgkmcnt(9)
	v_mfma_f32_16x16x32_f16 v[88:91], v[180:183], v[192:195], v[88:91]
	v_mfma_f32_16x16x32_f16 v[92:95], v[180:183], v[196:199], v[92:95]
	v_mfma_f32_16x16x32_f16 v[96:99], v[180:183], v[200:203], v[96:99]
	s_add_u32 m0, s28, 0x4000
	s_nop 0
	global_load_lds_dwordx4 v12, s[4:5]
	v_mfma_f32_16x16x32_f16 v[100:103], v[180:183], v[204:207], v[100:103]
	s_waitcnt lgkmcnt(8)
	v_mfma_f32_16x16x32_f16 v[104:107], v[184:187], v[192:195], v[104:107]
	v_mfma_f32_16x16x32_f16 v[108:111], v[184:187], v[196:199], v[108:111]
	v_mfma_f32_16x16x32_f16 v[112:115], v[184:187], v[200:203], v[112:115]
	v_mfma_f32_16x16x32_f16 v[116:119], v[184:187], v[204:207], v[116:119]
	s_waitcnt lgkmcnt(7)
	ds_read_b128 v[172:175], v16 offset:49152
	ds_read_b128 v[192:195], v18 offset:49152
	ds_read_b128 v[196:199], v18 offset:51200
	ds_read_b128 v[200:203], v18 offset:53248
	ds_read_b128 v[204:207], v18 offset:55296
	ds_read_b128 v[176:179], v16 offset:51200
	ds_read_b128 v[180:183], v16 offset:53248
	ds_read_b128 v[184:187], v16 offset:55296
	s_waitcnt lgkmcnt(14)
	v_mfma_f32_16x16x32_f16 v[56:59], v[136:139], v[156:159], v[56:59]
	s_add_u32 m0, s28, 0x6000
	s_nop 0
	global_load_lds_dwordx4 v13, s[4:5]
	s_add_u32 s4, s4, s20
	s_addc_u32 s5, s5, 0
	s_waitcnt lgkmcnt(13)
	v_mfma_f32_16x16x32_f16 v[60:63], v[136:139], v[160:163], v[60:63]
	s_waitcnt lgkmcnt(12)
	v_mfma_f32_16x16x32_f16 v[64:67], v[136:139], v[164:167], v[64:67]
	s_waitcnt lgkmcnt(11)
	v_mfma_f32_16x16x32_f16 v[68:71], v[136:139], v[168:171], v[68:71]
	s_waitcnt lgkmcnt(10)
	v_mfma_f32_16x16x32_f16 v[72:75], v[140:143], v[156:159], v[72:75]
	v_mfma_f32_16x16x32_f16 v[76:79], v[140:143], v[160:163], v[76:79]
	s_add_u32 m0, s28, 0x8000
	s_nop 0
	global_load_lds_dwordx4 v10, s[6:7]
	v_mfma_f32_16x16x32_f16 v[80:83], v[140:143], v[164:167], v[80:83]
	v_mfma_f32_16x16x32_f16 v[84:87], v[140:143], v[168:171], v[84:87]
	s_waitcnt lgkmcnt(9)
	v_mfma_f32_16x16x32_f16 v[88:91], v[144:147], v[156:159], v[88:91]
	v_mfma_f32_16x16x32_f16 v[92:95], v[144:147], v[160:163], v[92:95]
	v_mfma_f32_16x16x32_f16 v[96:99], v[144:147], v[164:167], v[96:99]
	s_add_u32 m0, s28, 0xa000
	s_nop 0
	global_load_lds_dwordx4 v11, s[6:7]
	s_add_u32 s6, s6, s20
	s_addc_u32 s7, s7, 0
	v_mfma_f32_16x16x32_f16 v[100:103], v[144:147], v[168:171], v[100:103]
	s_waitcnt lgkmcnt(8)
	v_mfma_f32_16x16x32_f16 v[104:107], v[148:151], v[156:159], v[104:107]
	v_mfma_f32_16x16x32_f16 v[108:111], v[148:151], v[160:163], v[108:111]
	v_mfma_f32_16x16x32_f16 v[112:115], v[148:151], v[164:167], v[112:115]
	v_mfma_f32_16x16x32_f16 v[116:119], v[148:151], v[168:171], v[116:119]
	s_waitcnt vmcnt(6) lgkmcnt(0)
	s_barrier
	s_waitcnt lgkmcnt(7)
	ds_read_b128 v[136:139], v19
	ds_read_b128 v[156:159], v21
	ds_read_b128 v[160:163], v21 offset:2048
	ds_read_b128 v[164:167], v21 offset:4096
	ds_read_b128 v[168:171], v21 offset:6144
	ds_read_b128 v[140:143], v19 offset:2048
	ds_read_b128 v[144:147], v19 offset:4096
	ds_read_b128 v[148:151], v19 offset:6144
	s_waitcnt lgkmcnt(14)
	v_mfma_f32_16x16x32_f16 v[56:59], v[172:175], v[192:195], v[56:59]
	s_waitcnt lgkmcnt(13)
	v_mfma_f32_16x16x32_f16 v[60:63], v[172:175], v[196:199], v[60:63]
	s_waitcnt lgkmcnt(12)
	v_mfma_f32_16x16x32_f16 v[64:67], v[172:175], v[200:203], v[64:67]
	s_waitcnt lgkmcnt(11)
	v_mfma_f32_16x16x32_f16 v[68:71], v[172:175], v[204:207], v[68:71]
	s_waitcnt lgkmcnt(10)
	v_mfma_f32_16x16x32_f16 v[72:75], v[176:179], v[192:195], v[72:75]
	v_mfma_f32_16x16x32_f16 v[76:79], v[176:179], v[196:199], v[76:79]
	v_mfma_f32_16x16x32_f16 v[80:83], v[176:179], v[200:203], v[80:83]
	v_mfma_f32_16x16x32_f16 v[84:87], v[176:179], v[204:207], v[84:87]
	s_waitcnt lgkmcnt(9)
	v_mfma_f32_16x16x32_f16 v[88:91], v[180:183], v[192:195], v[88:91]
	v_mfma_f32_16x16x32_f16 v[92:95], v[180:183], v[196:199], v[92:95]
	v_mfma_f32_16x16x32_f16 v[96:99], v[180:183], v[200:203], v[96:99]
	v_mfma_f32_16x16x32_f16 v[100:103], v[180:183], v[204:207], v[100:103]
	s_waitcnt lgkmcnt(8)
	v_mfma_f32_16x16x32_f16 v[104:107], v[184:187], v[192:195], v[104:107]
	v_mfma_f32_16x16x32_f16 v[108:111], v[184:187], v[196:199], v[108:111]
	v_mfma_f32_16x16x32_f16 v[112:115], v[184:187], v[200:203], v[112:115]
	v_mfma_f32_16x16x32_f16 v[116:119], v[184:187], v[204:207], v[116:119]
	s_waitcnt lgkmcnt(7)
	ds_read_b128 v[172:175], v20
	ds_read_b128 v[192:195], v22
	ds_read_b128 v[196:199], v22 offset:2048
	ds_read_b128 v[200:203], v22 offset:4096
	ds_read_b128 v[204:207], v22 offset:6144
	ds_read_b128 v[176:179], v20 offset:2048
	ds_read_b128 v[180:183], v20 offset:4096
	ds_read_b128 v[184:187], v20 offset:6144
	s_waitcnt lgkmcnt(14)
	v_mfma_f32_16x16x32_f16 v[56:59], v[136:139], v[156:159], v[56:59]
	s_waitcnt lgkmcnt(13)
	v_mfma_f32_16x16x32_f16 v[60:63], v[136:139], v[160:163], v[60:63]
	s_waitcnt lgkmcnt(12)
	v_mfma_f32_16x16x32_f16 v[64:67], v[136:139], v[164:167], v[64:67]
	s_waitcnt lgkmcnt(11)
	v_mfma_f32_16x16x32_f16 v[68:71], v[136:139], v[168:171], v[68:71]
	s_waitcnt lgkmcnt(10)
	v_mfma_f32_16x16x32_f16 v[72:75], v[140:143], v[156:159], v[72:75]
	v_mfma_f32_16x16x32_f16 v[76:79], v[140:143], v[160:163], v[76:79]
	v_mfma_f32_16x16x32_f16 v[80:83], v[140:143], v[164:167], v[80:83]
	v_mfma_f32_16x16x32_f16 v[84:87], v[140:143], v[168:171], v[84:87]
	s_waitcnt lgkmcnt(9)
	v_mfma_f32_16x16x32_f16 v[88:91], v[144:147], v[156:159], v[88:91]
	v_mfma_f32_16x16x32_f16 v[92:95], v[144:147], v[160:163], v[92:95]
	v_mfma_f32_16x16x32_f16 v[96:99], v[144:147], v[164:167], v[96:99]
	v_mfma_f32_16x16x32_f16 v[100:103], v[144:147], v[168:171], v[100:103]
	s_waitcnt lgkmcnt(8)
	v_mfma_f32_16x16x32_f16 v[104:107], v[148:151], v[156:159], v[104:107]
	v_mfma_f32_16x16x32_f16 v[108:111], v[148:151], v[160:163], v[108:111]
	v_mfma_f32_16x16x32_f16 v[112:115], v[148:151], v[164:167], v[112:115]
	v_mfma_f32_16x16x32_f16 v[116:119], v[148:151], v[168:171], v[116:119]
	s_waitcnt vmcnt(0) lgkmcnt(0)
	s_barrier
	s_waitcnt lgkmcnt(7)
	ds_read_b128 v[136:139], v15
	ds_read_b128 v[156:159], v17
	ds_read_b128 v[160:163], v17 offset:2048
	ds_read_b128 v[164:167], v17 offset:4096
	ds_read_b128 v[168:171], v17 offset:6144
	ds_read_b128 v[140:143], v15 offset:2048
	ds_read_b128 v[144:147], v15 offset:4096
	ds_read_b128 v[148:151], v15 offset:6144
	s_waitcnt lgkmcnt(14)
	v_mfma_f32_16x16x32_f16 v[56:59], v[172:175], v[192:195], v[56:59]
	s_waitcnt lgkmcnt(13)
	v_mfma_f32_16x16x32_f16 v[60:63], v[172:175], v[196:199], v[60:63]
	s_waitcnt lgkmcnt(12)
	v_mfma_f32_16x16x32_f16 v[64:67], v[172:175], v[200:203], v[64:67]
	s_waitcnt lgkmcnt(11)
	v_mfma_f32_16x16x32_f16 v[68:71], v[172:175], v[204:207], v[68:71]
	s_waitcnt lgkmcnt(10)
	v_mfma_f32_16x16x32_f16 v[72:75], v[176:179], v[192:195], v[72:75]
	v_mfma_f32_16x16x32_f16 v[76:79], v[176:179], v[196:199], v[76:79]
	v_mfma_f32_16x16x32_f16 v[80:83], v[176:179], v[200:203], v[80:83]
	v_mfma_f32_16x16x32_f16 v[84:87], v[176:179], v[204:207], v[84:87]
	s_waitcnt lgkmcnt(9)
	v_mfma_f32_16x16x32_f16 v[88:91], v[180:183], v[192:195], v[88:91]
	v_mfma_f32_16x16x32_f16 v[92:95], v[180:183], v[196:199], v[92:95]
	v_mfma_f32_16x16x32_f16 v[96:99], v[180:183], v[200:203], v[96:99]
	v_mfma_f32_16x16x32_f16 v[100:103], v[180:183], v[204:207], v[100:103]
	s_waitcnt lgkmcnt(8)
	v_mfma_f32_16x16x32_f16 v[104:107], v[184:187], v[192:195], v[104:107]
	v_mfma_f32_16x16x32_f16 v[108:111], v[184:187], v[196:199], v[108:111]
	v_mfma_f32_16x16x32_f16 v[112:115], v[184:187], v[200:203], v[112:115]
	v_mfma_f32_16x16x32_f16 v[116:119], v[184:187], v[204:207], v[116:119]
	s_waitcnt lgkmcnt(7)
	ds_read_b128 v[172:175], v16
	ds_read_b128 v[192:195], v18
	ds_read_b128 v[196:199], v18 offset:2048
	ds_read_b128 v[200:203], v18 offset:4096
	ds_read_b128 v[204:207], v18 offset:6144
	ds_read_b128 v[176:179], v16 offset:2048
	ds_read_b128 v[180:183], v16 offset:4096
	ds_read_b128 v[184:187], v16 offset:6144
	s_waitcnt lgkmcnt(14)
	v_mfma_f32_16x16x32_f16 v[56:59], v[136:139], v[156:159], v[56:59]
	s_waitcnt lgkmcnt(13)
	v_mfma_f32_16x16x32_f16 v[60:63], v[136:139], v[160:163], v[60:63]
	s_waitcnt lgkmcnt(12)
	v_mfma_f32_16x16x32_f16 v[64:67], v[136:139], v[164:167], v[64:67]
	s_waitcnt lgkmcnt(11)
	v_mfma_f32_16x16x32_f16 v[68:71], v[136:139], v[168:171], v[68:71]
	s_waitcnt lgkmcnt(10)
	v_mfma_f32_16x16x32_f16 v[72:75], v[140:143], v[156:159], v[72:75]
	v_mfma_f32_16x16x32_f16 v[76:79], v[140:143], v[160:163], v[76:79]
	v_mfma_f32_16x16x32_f16 v[80:83], v[140:143], v[164:167], v[80:83]
	v_mfma_f32_16x16x32_f16 v[84:87], v[140:143], v[168:171], v[84:87]
	s_waitcnt lgkmcnt(9)
	v_mfma_f32_16x16x32_f16 v[88:91], v[144:147], v[156:159], v[88:91]
	v_mfma_f32_16x16x32_f16 v[92:95], v[144:147], v[160:163], v[92:95]
	v_mfma_f32_16x16x32_f16 v[96:99], v[144:147], v[164:167], v[96:99]
	v_mfma_f32_16x16x32_f16 v[100:103], v[144:147], v[168:171], v[100:103]
	s_waitcnt lgkmcnt(8)
	v_mfma_f32_16x16x32_f16 v[104:107], v[148:151], v[156:159], v[104:107]
	v_mfma_f32_16x16x32_f16 v[108:111], v[148:151], v[160:163], v[108:111]
	v_mfma_f32_16x16x32_f16 v[112:115], v[148:151], v[164:167], v[112:115]
	v_mfma_f32_16x16x32_f16 v[116:119], v[148:151], v[168:171], v[116:119]
	s_waitcnt lgkmcnt(6)
	v_mfma_f32_16x16x32_f16 v[56:59], v[172:175], v[192:195], v[56:59]
	s_waitcnt lgkmcnt(5)
	v_mfma_f32_16x16x32_f16 v[60:63], v[172:175], v[196:199], v[60:63]
	s_waitcnt lgkmcnt(4)
	v_mfma_f32_16x16x32_f16 v[64:67], v[172:175], v[200:203], v[64:67]
	s_waitcnt lgkmcnt(3)
	v_mfma_f32_16x16x32_f16 v[68:71], v[172:175], v[204:207], v[68:71]
	s_waitcnt lgkmcnt(2)
	v_mfma_f32_16x16x32_f16 v[72:75], v[176:179], v[192:195], v[72:75]
	v_mfma_f32_16x16x32_f16 v[76:79], v[176:179], v[196:199], v[76:79]
	v_mfma_f32_16x16x32_f16 v[80:83], v[176:179], v[200:203], v[80:83]
	v_mfma_f32_16x16x32_f16 v[84:87], v[176:179], v[204:207], v[84:87]
	s_waitcnt lgkmcnt(1)
	v_mfma_f32_16x16x32_f16 v[88:91], v[180:183], v[192:195], v[88:91]
	v_mfma_f32_16x16x32_f16 v[92:95], v[180:183], v[196:199], v[92:95]
	v_mfma_f32_16x16x32_f16 v[96:99], v[180:183], v[200:203], v[96:99]
	v_mfma_f32_16x16x32_f16 v[100:103], v[180:183], v[204:207], v[100:103]
	s_waitcnt lgkmcnt(0)
	v_mfma_f32_16x16x32_f16 v[104:107], v[184:187], v[192:195], v[104:107]
	v_mfma_f32_16x16x32_f16 v[108:111], v[184:187], v[196:199], v[108:111]
	v_mfma_f32_16x16x32_f16 v[112:115], v[184:187], v[200:203], v[112:115]
	v_mfma_f32_16x16x32_f16 v[116:119], v[184:187], v[204:207], v[116:119]
	s_nop 7
	s_nop 1
	s_add_u32 s24, s29, 0
	s_lshl_b32 s8, s24, 11
	v_add_u32_e32 v212, s8, v23
	v_pk_add_f32 v[56:57], v[56:57], v[24:25] op_sel_hi:[1,0]
	v_pk_add_f32 v[58:59], v[58:59], v[24:25] op_sel_hi:[1,0]
	v_cvt_pk_f16_f32 v56, v56, v57
	v_cvt_pk_f16_f32 v57, v58, v59
	global_store_dwordx2 v212, v[56:57], s[22:23] offset:0
	v_pk_add_f32 v[60:61], v[60:61], v[26:27] op_sel_hi:[1,0]
	v_pk_add_f32 v[62:63], v[62:63], v[26:27] op_sel_hi:[1,0]
	v_cvt_pk_f16_f32 v60, v60, v61
	v_cvt_pk_f16_f32 v61, v62, v63
	global_store_dwordx2 v212, v[60:61], s[22:23] offset:256
	v_pk_add_f32 v[64:65], v[64:65], v[28:29] op_sel_hi:[1,0]
	v_pk_add_f32 v[66:67], v[66:67], v[28:29] op_sel_hi:[1,0]
	v_cvt_pk_f16_f32 v64, v64, v65
	v_cvt_pk_f16_f32 v65, v66, v67
	global_store_dwordx2 v212, v[64:65], s[22:23] offset:1024
	v_pk_add_f32 v[68:69], v[68:69], v[30:31] op_sel_hi:[1,0]
	v_pk_add_f32 v[70:71], v[70:71], v[30:31] op_sel_hi:[1,0]
	v_cvt_pk_f16_f32 v68, v68, v69
	v_cvt_pk_f16_f32 v69, v70, v71
	global_store_dwordx2 v212, v[68:69], s[22:23] offset:1280
	s_add_u32 s24, s29, 1
	s_lshl_b32 s8, s24, 11
	v_add_u32_e32 v212, s8, v23
	v_pk_add_f32 v[72:73], v[72:73], v[24:25] op_sel_hi:[1,0]
	v_pk_add_f32 v[74:75], v[74:75], v[24:25] op_sel_hi:[1,0]
	v_cvt_pk_f16_f32 v72, v72, v73
	v_cvt_pk_f16_f32 v73, v74, v75
	global_store_dwordx2 v212, v[72:73], s[22:23] offset:0
	v_pk_add_f32 v[76:77], v[76:77], v[26:27] op_sel_hi:[1,0]
	v_pk_add_f32 v[78:79], v[78:79], v[26:27] op_sel_hi:[1,0]
	v_cvt_pk_f16_f32 v76, v76, v77
	v_cvt_pk_f16_f32 v77, v78, v79
	global_store_dwordx2 v212, v[76:77], s[22:23] offset:256
	v_pk_add_f32 v[80:81], v[80:81], v[28:29] op_sel_hi:[1,0]
	v_pk_add_f32 v[82:83], v[82:83], v[28:29] op_sel_hi:[1,0]
	v_cvt_pk_f16_f32 v80, v80, v81
	v_cvt_pk_f16_f32 v81, v82, v83
	global_store_dwordx2 v212, v[80:81], s[22:23] offset:1024
	v_pk_add_f32 v[84:85], v[84:85], v[30:31] op_sel_hi:[1,0]
	v_pk_add_f32 v[86:87], v[86:87], v[30:31] op_sel_hi:[1,0]
	v_cvt_pk_f16_f32 v84, v84, v85
	v_cvt_pk_f16_f32 v85, v86, v87
	global_store_dwordx2 v212, v[84:85], s[22:23] offset:1280
	s_add_u32 s24, s29, 2
	s_lshl_b32 s8, s24, 11
	v_add_u32_e32 v212, s8, v23
	v_pk_add_f32 v[88:89], v[88:89], v[24:25] op_sel_hi:[1,0]
	v_pk_add_f32 v[90:91], v[90:91], v[24:25] op_sel_hi:[1,0]
	v_cvt_pk_f16_f32 v88, v88, v89
	v_cvt_pk_f16_f32 v89, v90, v91
	global_store_dwordx2 v212, v[88:89], s[22:23] offset:0
	v_pk_add_f32 v[92:93], v[92:93], v[26:27] op_sel_hi:[1,0]
	v_pk_add_f32 v[94:95], v[94:95], v[26:27] op_sel_hi:[1,0]
	v_cvt_pk_f16_f32 v92, v92, v93
	v_cvt_pk_f16_f32 v93, v94, v95
	global_store_dwordx2 v212, v[92:93], s[22:23] offset:256
	v_pk_add_f32 v[96:97], v[96:97], v[28:29] op_sel_hi:[1,0]
	v_pk_add_f32 v[98:99], v[98:99], v[28:29] op_sel_hi:[1,0]
	v_cvt_pk_f16_f32 v96, v96, v97
	v_cvt_pk_f16_f32 v97, v98, v99
	global_store_dwordx2 v212, v[96:97], s[22:23] offset:1024
	v_pk_add_f32 v[100:101], v[100:101], v[30:31] op_sel_hi:[1,0]
	v_pk_add_f32 v[102:103], v[102:103], v[30:31] op_sel_hi:[1,0]
	v_cvt_pk_f16_f32 v100, v100, v101
	v_cvt_pk_f16_f32 v101, v102, v103
	global_store_dwordx2 v212, v[100:101], s[22:23] offset:1280
	s_add_u32 s24, s29, 3
	s_lshl_b32 s8, s24, 11
	v_add_u32_e32 v212, s8, v23
	v_pk_add_f32 v[104:105], v[104:105], v[24:25] op_sel_hi:[1,0]
	v_pk_add_f32 v[106:107], v[106:107], v[24:25] op_sel_hi:[1,0]
	v_cvt_pk_f16_f32 v104, v104, v105
	v_cvt_pk_f16_f32 v105, v106, v107
	global_store_dwordx2 v212, v[104:105], s[22:23] offset:0
	v_pk_add_f32 v[108:109], v[108:109], v[26:27] op_sel_hi:[1,0]
	v_pk_add_f32 v[110:111], v[110:111], v[26:27] op_sel_hi:[1,0]
	v_cvt_pk_f16_f32 v108, v108, v109
	v_cvt_pk_f16_f32 v109, v110, v111
	global_store_dwordx2 v212, v[108:109], s[22:23] offset:256
	v_pk_add_f32 v[112:113], v[112:113], v[28:29] op_sel_hi:[1,0]
	v_pk_add_f32 v[114:115], v[114:115], v[28:29] op_sel_hi:[1,0]
	v_cvt_pk_f16_f32 v112, v112, v113
	v_cvt_pk_f16_f32 v113, v114, v115
	global_store_dwordx2 v212, v[112:113], s[22:23] offset:1024
	v_pk_add_f32 v[116:117], v[116:117], v[30:31] op_sel_hi:[1,0]
	v_pk_add_f32 v[118:119], v[118:119], v[30:31] op_sel_hi:[1,0]
	v_cvt_pk_f16_f32 v116, v116, v117
	v_cvt_pk_f16_f32 v117, v118, v119
	global_store_dwordx2 v212, v[116:117], s[22:23] offset:1280
	s_branch .Lpf_done
